# E35: E34 (route read pipelining depth 1) + route norm/modulation vectors loaded once per workgroup instead of per token pair (removes 8 serialized L2 round trips per pair)
# speedup vs baseline: 1.0166x; 1.0022x over previous
.LBB0_1358:
	s_and_saveexec_b64 s[0:1], s[38:39]
	ds_write_b32 v155, v101
	s_or_b64 exec, exec, s[0:1]
	s_lshl_b32 s0, s26, 6
	s_add_i32 s0, s0, s24
	s_ashr_i32 s1, s0, 31
	s_lshl_b64 s[6:7], s[0:1], 11
	s_or_b32 s0, s0, 1
	s_ashr_i32 s1, s0, 31
	v_lshl_add_u64 v[2:3], v[14:15], 0, s[6:7]
	s_lshl_b64 s[0:1], s[0:1], 11
	s_waitcnt lgkmcnt(0)
	s_barrier
	s_add_i32 s100, s25, -3
	s_ashr_i32 s100, s100, 12
	s_add_i32 s100, s100, s16
	s_mul_hi_i32 s101, s100, 0x6000
	s_mulk_i32 s100, 0x6000
	s_add_u32 s100, s2, s100
	s_addc_u32 s101, s3, s101
	s_add_u32 s12, s100, 0x103000
	s_addc_u32 s13, s101, 0
	s_add_u32 s14, s100, 0x104000
	s_addc_u32 s15, s101, 0
	global_load_dwordx4 v[174:177], v[16:17], off
	global_load_dwordx4 v[190:193], v160, s[14:15]
	global_load_dwordx4 v[236:239], v160, s[12:13]
	global_load_dwordx4 v[178:181], v[16:17], off offset:1024
	global_load_dwordx4 v[202:205], v161, s[14:15]
	global_load_dwordx4 v[240:243], v161, s[12:13]
	global_load_dwordx4 v[182:185], v[16:17], off offset:2048
	global_load_dwordx4 v[206:209], v162, s[14:15]
	global_load_dwordx4 v[244:247], v162, s[12:13]
	global_load_dwordx4 v[186:189], v[16:17], off offset:3072
	global_load_dwordx4 v[232:235], v163, s[14:15]
	global_load_dwordx2 v[216:217], v163, s[12:13]
	global_load_dwordx2 v[228:229], v163, s[12:13] offset:8
	global_load_dwordx2 v[24:25], v[2:3], off
	global_load_dwordx2 v[26:27], v[2:3], off offset:512
	global_load_dwordx2 v[28:29], v[2:3], off offset:1024
	global_load_dwordx2 v[30:31], v[2:3], off offset:1536
	v_lshl_add_u64 v[2:3], v[14:15], 0, s[0:1]
	global_load_dwordx2 v[32:33], v[2:3], off
	global_load_dwordx2 v[34:35], v[2:3], off offset:512
	global_load_dwordx2 v[36:37], v[2:3], off offset:1024
	global_load_dwordx2 v[38:39], v[2:3], off offset:1536
	s_mov_b32 s27, 0
	s_mov_b32 s6, s25
	s_waitcnt vmcnt(8)
	v_pk_add_f32 v[190:191], v[190:191], 1.0 op_sel_hi:[1,0]
	v_pk_add_f32 v[192:193], v[192:193], 1.0 op_sel_hi:[1,0]
	v_pk_add_f32 v[202:203], v[202:203], 1.0 op_sel_hi:[1,0]
	v_pk_add_f32 v[204:205], v[204:205], 1.0 op_sel_hi:[1,0]
	v_pk_add_f32 v[206:207], v[206:207], 1.0 op_sel_hi:[1,0]
	v_pk_add_f32 v[208:209], v[208:209], 1.0 op_sel_hi:[1,0]
	v_pk_add_f32 v[232:233], v[232:233], 1.0 op_sel_hi:[1,0]
	v_pk_add_f32 v[234:235], v[234:235], 1.0 op_sel_hi:[1,0]
	s_branch .LBB0_1362

.LBB0_1362:
	s_waitcnt vmcnt(7)
	v_and_b32_e32 v47, 0xffff0000, v24
	v_and_b32_e32 v49, 0xffff0000, v25
	v_lshlrev_b32_e32 v46, 16, v24
	v_lshlrev_b32_e32 v48, 16, v25
	v_mul_f32_e32 v2, v47, v47
	v_mul_f32_e32 v3, v49, v49
	v_fmac_f32_e32 v2, v46, v46
	v_fmac_f32_e32 v3, v48, v48
	s_waitcnt vmcnt(6)
	v_and_b32_e32 v53, 0xffff0000, v26
	v_and_b32_e32 v51, 0xffff0000, v27
	v_add_f32_e32 v2, v2, v3
	v_lshlrev_b32_e32 v52, 16, v26
	v_lshlrev_b32_e32 v50, 16, v27
	v_mul_f32_e32 v3, v53, v53
	v_mul_f32_e32 v4, v51, v51
	v_fmac_f32_e32 v3, v52, v52
	v_fmac_f32_e32 v4, v50, v50
	v_add_f32_e32 v3, v3, v4
	s_waitcnt vmcnt(5)
	v_and_b32_e32 v55, 0xffff0000, v28
	v_and_b32_e32 v45, 0xffff0000, v29
	v_add_f32_e32 v2, v3, v2
	v_lshlrev_b32_e32 v54, 16, v28
	v_lshlrev_b32_e32 v44, 16, v29
	v_mul_f32_e32 v3, v55, v55
	v_mul_f32_e32 v4, v45, v45
	v_fmac_f32_e32 v3, v54, v54
	v_fmac_f32_e32 v4, v44, v44
	v_add_f32_e32 v3, v3, v4
	s_waitcnt vmcnt(4)
	v_and_b32_e32 v41, 0xffff0000, v30
	v_and_b32_e32 v43, 0xffff0000, v31
	v_add_f32_e32 v2, v3, v2
	v_lshlrev_b32_e32 v40, 16, v30
	v_lshlrev_b32_e32 v42, 16, v31
	v_mul_f32_e32 v3, v41, v41
	v_mul_f32_e32 v4, v43, v43
	v_fmac_f32_e32 v3, v40, v40
	v_fmac_f32_e32 v4, v42, v42
	v_add_f32_e32 v3, v3, v4
	v_add_f32_e32 v2, v3, v2
	s_add_i32 s8, s6, -3
	s_ashr_i32 s0, s8, 12
	v_add_f32_dpp v2, v2, v2 quad_perm:[1,0,3,2] row_mask:0xf bank_mask:0xf bound_ctrl:1
	s_add_i32 s0, s0, s16
	s_mul_hi_i32 s1, s0, 0x6000
	v_add_f32_dpp v2, v2, v2 quad_perm:[2,3,0,1] row_mask:0xf bank_mask:0xf bound_ctrl:1
	s_mulk_i32 s0, 0x6000
	s_add_u32 s0, s2, s0
	v_add_f32_dpp v2, v2, v2 row_half_mirror row_mask:0xf bank_mask:0xf bound_ctrl:1
	s_addc_u32 s1, s3, s1
	s_add_u32 s12, s0, 0x103000
	v_add_f32_dpp v2, v2, v2 row_mirror row_mask:0xf bank_mask:0xf bound_ctrl:1
	v_mov_b32_e32 v3, v2
	s_nop 1
	v_permlane16_swap_b32_e32 v2, v3
	v_add_f32_e32 v2, v2, v3
	v_mov_b32_e32 v3, v2
	s_nop 1
	v_permlane32_swap_b32_e32 v2, v3
	v_add_f32_e32 v2, v2, v3
	v_fmamk_f32 v2, v2, 0x3a800000, v215
	v_cmp_gt_f32_e32 vcc, s59, v2
	v_mul_f32_e32 v3, 0x4f800000, v2
	s_addc_u32 s13, s1, 0
	v_cndmask_b32_e32 v2, v2, v3, vcc
	v_sqrt_f32_e32 v3, v2
	s_add_u32 s14, s0, 0x104000
	s_addc_u32 s15, s1, 0
	s_ashr_i32 s9, s8, 31
	v_add_u32_e32 v4, -1, v3
	v_fma_f32 v5, -v4, v3, v2
	v_cmp_ge_f32_e64 s[0:1], 0, v5
	v_add_u32_e32 v5, 1, v3
	s_add_i32 s10, s6, -2
	v_cndmask_b32_e64 v4, v3, v4, s[0:1]
	v_fma_f32 v3, -v5, v3, v2
	v_cmp_lt_f32_e64 s[0:1], 0, v3
	s_ashr_i32 s11, s10, 31
	s_nop 0
	v_cndmask_b32_e64 v3, v4, v5, s[0:1]
	v_mul_f32_e32 v4, 0x37800000, v3
	v_cndmask_b32_e32 v3, v3, v4, vcc
	v_cmp_class_f32_e32 vcc, v2, v212
	s_nop 1
	v_cndmask_b32_e32 v2, v3, v2, vcc
	v_div_scale_f32 v3, s[0:1], v2, v2, 1.0
	v_rcp_f32_e32 v4, v3
	s_lshl_b64 s[0:1], s[8:9], 11
	v_lshl_add_u64 v[62:63], v[22:23], 0, s[0:1]
	v_fma_f32 v5, -v3, v4, 1.0
	v_fmac_f32_e32 v4, v5, v4
	v_div_scale_f32 v5, vcc, 1.0, v2, 1.0
	v_mul_f32_e32 v6, v5, v4
	v_fma_f32 v7, -v3, v6, v5
	v_fmac_f32_e32 v6, v7, v4
	v_fma_f32 v3, -v3, v6, v5
	v_div_fmas_f32 v3, v3, v4, v6
	v_div_fixup_f32 v58, v3, v2, 1.0
	v_pk_mul_f32 v[48:49], v[58:59], v[48:49] op_sel_hi:[0,1]
	v_pk_mul_f32 v[46:47], v[58:59], v[46:47] op_sel_hi:[0,1]
	v_pk_mul_f32 v[52:53], v[58:59], v[52:53] op_sel_hi:[0,1]
	v_pk_mul_f32 v[50:51], v[58:59], v[50:51] op_sel_hi:[0,1]
	v_pk_mul_f32 v[54:55], v[58:59], v[54:55] op_sel_hi:[0,1]
	v_pk_mul_f32 v[44:45], v[58:59], v[44:45] op_sel_hi:[0,1]
	v_pk_mul_f32 v[40:41], v[58:59], v[40:41] op_sel_hi:[0,1]
	v_pk_mul_f32 v[42:43], v[58:59], v[42:43] op_sel_hi:[0,1]
	v_pk_mul_f32 v[2:3], v[174:175], v[46:47]
	v_pk_mul_f32 v[4:5], v[176:177], v[48:49]
	s_waitcnt vmcnt(0)
	v_pk_fma_f32 v[48:49], v[192:193], v[4:5], v[238:239]
	v_pk_fma_f32 v[46:47], v[190:191], v[2:3], v[236:237]
	v_cvt_pk_bf16_f32 v3, v48, v49
	v_cvt_pk_bf16_f32 v2, v46, v47
	global_store_dwordx2 v[62:63], v[2:3], off
	v_pk_mul_f32 v[4:5], v[180:181], v[50:51]
	v_pk_mul_f32 v[2:3], v[178:179], v[52:53]
	v_pk_fma_f32 v[52:53], v[204:205], v[4:5], v[242:243]
	v_pk_fma_f32 v[50:51], v[202:203], v[2:3], v[240:241]
	v_cvt_pk_bf16_f32 v3, v52, v53
	v_cvt_pk_bf16_f32 v2, v50, v51
	global_store_dwordx2 v[62:63], v[2:3], off offset:512
	v_pk_mul_f32 v[4:5], v[184:185], v[44:45]
	v_pk_mul_f32 v[2:3], v[182:183], v[54:55]
	v_pk_fma_f32 v[56:57], v[208:209], v[4:5], v[246:247]
	v_pk_fma_f32 v[54:55], v[206:207], v[2:3], v[244:245]
	v_cvt_pk_bf16_f32 v3, v56, v57
	v_cvt_pk_bf16_f32 v2, v54, v55
	global_store_dwordx2 v[62:63], v[2:3], off offset:1024
	v_pk_mul_f32 v[4:5], v[42:43], v[188:189]
	v_pk_mul_f32 v[2:3], v[40:41], v[186:187]
	v_pk_fma_f32 v[60:61], v[4:5], v[234:235], v[228:229]
	v_pk_fma_f32 v[58:59], v[2:3], v[232:233], v[216:217]
	v_cvt_pk_bf16_f32 v3, v60, v61
	v_cvt_pk_bf16_f32 v2, v58, v59
	global_store_dwordx2 v[62:63], v[2:3], off offset:1536
	v_and_b32_e32 v3, 0xffff0000, v32
	v_and_b32_e32 v5, 0xffff0000, v33
	v_lshlrev_b32_e32 v2, 16, v32
	v_lshlrev_b32_e32 v4, 16, v33
	v_mul_f32_e32 v6, v3, v3
	v_mul_f32_e32 v7, v5, v5
	v_fmac_f32_e32 v6, v2, v2
	v_fmac_f32_e32 v7, v4, v4
	v_and_b32_e32 v13, 0xffff0000, v34
	v_and_b32_e32 v11, 0xffff0000, v35
	v_add_f32_e32 v6, v6, v7
	v_lshlrev_b32_e32 v12, 16, v34
	v_lshlrev_b32_e32 v10, 16, v35
	v_mul_f32_e32 v7, v13, v13
	v_mul_f32_e32 v8, v11, v11
	v_fmac_f32_e32 v7, v12, v12
	v_fmac_f32_e32 v8, v10, v10
	v_add_f32_e32 v7, v7, v8
	v_and_b32_e32 v43, 0xffff0000, v36
	v_and_b32_e32 v41, 0xffff0000, v37
	v_add_f32_e32 v6, v7, v6
	v_lshlrev_b32_e32 v42, 16, v36
	v_lshlrev_b32_e32 v40, 16, v37
	v_mul_f32_e32 v7, v43, v43
	v_mul_f32_e32 v8, v41, v41
	v_fmac_f32_e32 v7, v42, v42
	v_fmac_f32_e32 v8, v40, v40
	v_add_f32_e32 v7, v7, v8
	v_add_f32_e32 v44, v7, v6
	v_and_b32_e32 v9, 0xffff0000, v38
	v_and_b32_e32 v7, 0xffff0000, v39
	v_lshlrev_b32_e32 v8, 16, v38
	v_lshlrev_b32_e32 v6, 16, v39
	v_mul_f32_e32 v45, v9, v9
	v_mul_f32_e32 v62, v7, v7
	v_fmac_f32_e32 v45, v8, v8
	v_fmac_f32_e32 v62, v6, v6
	v_add_f32_e32 v45, v45, v62
	v_add_f32_e32 v44, v45, v44
	s_nop 1
	v_add_f32_dpp v44, v44, v44 quad_perm:[1,0,3,2] row_mask:0xf bank_mask:0xf bound_ctrl:1
	s_nop 1
	v_add_f32_dpp v44, v44, v44 quad_perm:[2,3,0,1] row_mask:0xf bank_mask:0xf bound_ctrl:1
	s_nop 1
	v_add_f32_dpp v44, v44, v44 row_half_mirror row_mask:0xf bank_mask:0xf bound_ctrl:1
	s_nop 1
	v_add_f32_dpp v44, v44, v44 row_mirror row_mask:0xf bank_mask:0xf bound_ctrl:1
	v_mov_b32_e32 v45, v44
	s_nop 1
	v_permlane16_swap_b32_e32 v44, v45
	v_add_f32_e32 v44, v44, v45
	v_mov_b32_e32 v45, v44
	s_nop 1
	v_permlane32_swap_b32_e32 v44, v45
	v_add_f32_e32 v44, v44, v45
	v_fmamk_f32 v44, v44, 0x3a800000, v215
	v_cmp_gt_f32_e32 vcc, s59, v44
	v_mul_f32_e32 v45, 0x4f800000, v44
	s_nop 0
	v_cndmask_b32_e32 v44, v44, v45, vcc
	v_sqrt_f32_e32 v45, v44
	s_nop 0
	v_add_u32_e32 v62, -1, v45
	v_fma_f32 v63, -v62, v45, v44
	v_cmp_ge_f32_e64 s[0:1], 0, v63
	v_add_u32_e32 v63, 1, v45
	s_nop 0
	v_cndmask_b32_e64 v62, v45, v62, s[0:1]
	v_fma_f32 v45, -v63, v45, v44
	v_cmp_lt_f32_e64 s[0:1], 0, v45
	s_nop 1
	v_cndmask_b32_e64 v45, v62, v63, s[0:1]
	v_mul_f32_e32 v62, 0x37800000, v45
	v_cndmask_b32_e32 v45, v45, v62, vcc
	v_cmp_class_f32_e32 vcc, v44, v212
	s_nop 1
	v_cndmask_b32_e32 v44, v45, v44, vcc
	v_div_scale_f32 v45, s[0:1], v44, v44, 1.0
	v_rcp_f32_e32 v62, v45
	s_lshl_b64 s[0:1], s[10:11], 11
	v_lshl_add_u64 v[74:75], v[22:23], 0, s[0:1]
	s_cmpk_eq_i32 s27, 0x60
	v_fma_f32 v63, -v45, v62, 1.0
	v_fmac_f32_e32 v62, v63, v62
	v_div_scale_f32 v63, vcc, 1.0, v44, 1.0
	v_mul_f32_e32 v64, v63, v62
	v_fma_f32 v65, -v45, v64, v63
	v_fmac_f32_e32 v64, v65, v62
	v_fma_f32 v45, -v45, v64, v63
	v_div_fmas_f32 v45, v45, v62, v64
	v_div_fixup_f32 v44, v45, v44, 1.0
	v_pk_mul_f32 v[2:3], v[44:45], v[2:3] op_sel_hi:[0,1]
	v_pk_mul_f32 v[4:5], v[44:45], v[4:5] op_sel_hi:[0,1]
	v_pk_mul_f32 v[12:13], v[44:45], v[12:13] op_sel_hi:[0,1]
	v_pk_mul_f32 v[10:11], v[44:45], v[10:11] op_sel_hi:[0,1]
	v_pk_mul_f32 v[42:43], v[44:45], v[42:43] op_sel_hi:[0,1]
	v_pk_mul_f32 v[40:41], v[44:45], v[40:41] op_sel_hi:[0,1]
	v_pk_mul_f32 v[8:9], v[44:45], v[8:9] op_sel_hi:[0,1]
	v_pk_mul_f32 v[6:7], v[44:45], v[6:7] op_sel_hi:[0,1]
	v_pk_mul_f32 v[64:65], v[176:177], v[4:5]
	v_pk_mul_f32 v[2:3], v[174:175], v[2:3]
	v_pk_add_f32 v[62:63], v[192:193], 0 op_sel_hi:[1,0]
	v_pk_add_f32 v[4:5], v[190:191], 0 op_sel_hi:[1,0]
	v_pk_fma_f32 v[4:5], v[4:5], v[2:3], v[236:237]
	v_pk_fma_f32 v[2:3], v[62:63], v[64:65], v[238:239]
	v_cvt_pk_bf16_f32 v62, v4, v5
	v_cvt_pk_bf16_f32 v63, v2, v3
	global_store_dwordx2 v[74:75], v[62:63], off
	v_pk_mul_f32 v[10:11], v[180:181], v[10:11]
	v_pk_mul_f32 v[12:13], v[178:179], v[12:13]
	v_pk_add_f32 v[62:63], v[204:205], 0 op_sel_hi:[1,0]
	v_pk_add_f32 v[64:65], v[202:203], 0 op_sel_hi:[1,0]
	v_pk_fma_f32 v[10:11], v[62:63], v[10:11], v[242:243]
	v_pk_fma_f32 v[12:13], v[64:65], v[12:13], v[240:241]
	v_cvt_pk_bf16_f32 v63, v10, v11
	v_cvt_pk_bf16_f32 v62, v12, v13
	global_store_dwordx2 v[74:75], v[62:63], off offset:512
	v_pk_mul_f32 v[40:41], v[184:185], v[40:41]
	v_pk_mul_f32 v[42:43], v[182:183], v[42:43]
	v_pk_add_f32 v[62:63], v[208:209], 0 op_sel_hi:[1,0]
	v_pk_add_f32 v[64:65], v[206:207], 0 op_sel_hi:[1,0]
	v_pk_fma_f32 v[40:41], v[62:63], v[40:41], v[246:247]
	v_pk_fma_f32 v[42:43], v[64:65], v[42:43], v[244:245]
	v_cvt_pk_bf16_f32 v63, v40, v41
	v_cvt_pk_bf16_f32 v62, v42, v43
	global_store_dwordx2 v[74:75], v[62:63], off offset:1024
	v_pk_mul_f32 v[6:7], v[6:7], v[188:189]
	v_pk_mul_f32 v[8:9], v[8:9], v[186:187]
	v_pk_add_f32 v[44:45], v[234:235], 0 op_sel_hi:[1,0]
	v_pk_add_f32 v[62:63], v[232:233], 0 op_sel_hi:[1,0]
	v_pk_fma_f32 v[6:7], v[6:7], v[44:45], v[228:229]
	v_pk_fma_f32 v[8:9], v[8:9], v[62:63], v[216:217]
	v_cvt_pk_bf16_f32 v45, v6, v7
	v_cvt_pk_bf16_f32 v44, v8, v9
	global_store_dwordx2 v[74:75], v[44:45], off offset:1536
	s_cbranch_scc1 .LBB0_1364
	s_add_i32 s0, s6, -1
	s_ashr_i32 s1, s0, 31
	s_lshl_b64 s[0:1], s[0:1], 11
	s_ashr_i32 s7, s6, 31
	v_lshl_add_u64 v[30:31], v[14:15], 0, s[0:1]
	s_lshl_b64 s[0:1], s[6:7], 11
	v_lshl_add_u64 v[38:39], v[14:15], 0, s[0:1]
	global_load_dwordx2 v[24:25], v[30:31], off
	global_load_dwordx2 v[26:27], v[30:31], off offset:512
	global_load_dwordx2 v[28:29], v[30:31], off offset:1024
	s_nop 0
	global_load_dwordx2 v[30:31], v[30:31], off offset:1536
	s_nop 0
	global_load_dwordx2 v[32:33], v[38:39], off
	global_load_dwordx2 v[34:35], v[38:39], off offset:512
	global_load_dwordx2 v[36:37], v[38:39], off offset:1024
	s_nop 0
	global_load_dwordx2 v[38:39], v[38:39], off offset:1536
.LBB0_1364:
	ds_read_b128 v[194:197], v89
	ds_read_b128 v[198:201], v89 offset:1024
	v_mov_b32_e32 v44, v46
	v_mov_b32_e32 v45, v4
	v_mov_b32_e32 v4, v47
	v_mov_b32_e32 v46, v48
	s_waitcnt lgkmcnt(1)
	v_pk_fma_f32 v[66:67], v[44:45], v[194:195], 0 op_sel_hi:[1,0,0]
	v_mov_b32_e32 v47, v2
	v_pk_fma_f32 v[62:63], v[4:5], v[194:195], v[66:67] op_sel:[0,1,0]
	v_mov_b32_e32 v2, v49
	v_pk_fma_f32 v[62:63], v[46:47], v[196:197], v[62:63] op_sel_hi:[1,0,1]
	v_mov_b32_e32 v48, v197
	v_pk_fma_f32 v[66:67], v[2:3], v[48:49], v[62:63] op_sel_hi:[1,0,1]
	ds_read_b128 v[194:197], v89 offset:2048
	v_mov_b32_e32 v48, v50
	v_mov_b32_e32 v49, v12
	v_mov_b32_e32 v12, v51
	v_mov_b32_e32 v50, v52
	s_waitcnt lgkmcnt(1)
	v_pk_fma_f32 v[66:67], v[48:49], v[198:199], v[66:67] op_sel_hi:[1,0,1]
	v_mov_b32_e32 v51, v10
	v_pk_fma_f32 v[62:63], v[12:13], v[198:199], v[66:67] op_sel:[0,1,0]
	v_mov_b32_e32 v10, v53
	v_pk_fma_f32 v[62:63], v[50:51], v[200:201], v[62:63] op_sel_hi:[1,0,1]
	v_mov_b32_e32 v52, v201
	v_pk_fma_f32 v[66:67], v[10:11], v[52:53], v[62:63] op_sel_hi:[1,0,1]
	ds_read_b128 v[198:201], v89 offset:3072
	v_mov_b32_e32 v52, v54
	v_mov_b32_e32 v53, v42
	v_mov_b32_e32 v42, v55
	v_mov_b32_e32 v54, v56
	s_waitcnt lgkmcnt(1)
	v_pk_fma_f32 v[66:67], v[52:53], v[194:195], v[66:67] op_sel_hi:[1,0,1]
	v_mov_b32_e32 v55, v40
	v_pk_fma_f32 v[62:63], v[42:43], v[194:195], v[66:67] op_sel:[0,1,0]
	v_mov_b32_e32 v40, v57
	v_pk_fma_f32 v[62:63], v[54:55], v[196:197], v[62:63] op_sel_hi:[1,0,1]
	v_mov_b32_e32 v56, v197
	v_pk_fma_f32 v[66:67], v[40:41], v[56:57], v[62:63] op_sel_hi:[1,0,1]
	ds_read_b128 v[194:197], v89 offset:4096
	v_mov_b32_e32 v56, v58
	v_mov_b32_e32 v57, v8
	v_mov_b32_e32 v8, v59
	v_mov_b32_e32 v58, v60
	s_waitcnt lgkmcnt(1)
	v_pk_fma_f32 v[66:67], v[56:57], v[198:199], v[66:67] op_sel_hi:[1,0,1]
	v_mov_b32_e32 v59, v6
	v_pk_fma_f32 v[62:63], v[8:9], v[198:199], v[66:67] op_sel:[0,1,0]
	v_mov_b32_e32 v6, v61
	v_pk_fma_f32 v[62:63], v[58:59], v[200:201], v[62:63] op_sel_hi:[1,0,1]
	v_mov_b32_e32 v60, v201
	v_pk_fma_f32 v[60:61], v[6:7], v[60:61], v[62:63] op_sel_hi:[1,0,1]
	ds_read_b128 v[198:201], v89 offset:5120
	s_waitcnt lgkmcnt(1)
	v_pk_fma_f32 v[66:67], v[44:45], v[194:195], 0 op_sel_hi:[1,0,0]
	s_nop 0
	v_pk_fma_f32 v[62:63], v[4:5], v[194:195], v[66:67] op_sel:[0,1,0]
	s_nop 0
	v_pk_fma_f32 v[62:63], v[46:47], v[196:197], v[62:63] op_sel_hi:[1,0,1]
	v_mov_b32_e32 v196, v197
	v_pk_fma_f32 v[66:67], v[2:3], v[196:197], v[62:63] op_sel_hi:[1,0,1]
	ds_read_b128 v[194:197], v89 offset:6144
	s_waitcnt lgkmcnt(1)
	v_pk_fma_f32 v[66:67], v[48:49], v[198:199], v[66:67] op_sel_hi:[1,0,1]
	s_nop 0
	v_pk_fma_f32 v[62:63], v[12:13], v[198:199], v[66:67] op_sel:[0,1,0]
	s_nop 0
	v_pk_fma_f32 v[62:63], v[50:51], v[200:201], v[62:63] op_sel_hi:[1,0,1]
	v_mov_b32_e32 v200, v201
	v_pk_fma_f32 v[66:67], v[10:11], v[200:201], v[62:63] op_sel_hi:[1,0,1]
	ds_read_b128 v[198:201], v89 offset:7168
	s_waitcnt lgkmcnt(1)
	v_pk_fma_f32 v[66:67], v[52:53], v[194:195], v[66:67] op_sel_hi:[1,0,1]
	s_nop 0
	v_pk_fma_f32 v[62:63], v[42:43], v[194:195], v[66:67] op_sel:[0,1,0]
	s_nop 0
	v_pk_fma_f32 v[62:63], v[54:55], v[196:197], v[62:63] op_sel_hi:[1,0,1]
	v_mov_b32_e32 v196, v197
	v_pk_fma_f32 v[66:67], v[40:41], v[196:197], v[62:63] op_sel_hi:[1,0,1]
	ds_read_b128 v[194:197], v89 offset:8192
	s_waitcnt lgkmcnt(1)
	v_pk_fma_f32 v[66:67], v[56:57], v[198:199], v[66:67] op_sel_hi:[1,0,1]
	s_nop 0
	v_pk_fma_f32 v[62:63], v[8:9], v[198:199], v[66:67] op_sel:[0,1,0]
	s_nop 0
	v_pk_fma_f32 v[62:63], v[58:59], v[200:201], v[62:63] op_sel_hi:[1,0,1]
	v_mov_b32_e32 v200, v201
	v_pk_fma_f32 v[62:63], v[6:7], v[200:201], v[62:63] op_sel_hi:[1,0,1]
	ds_read_b128 v[198:201], v89 offset:9216
	s_waitcnt lgkmcnt(1)
	v_pk_fma_f32 v[68:69], v[44:45], v[194:195], 0 op_sel_hi:[1,0,0]
	s_nop 0
	v_pk_fma_f32 v[64:65], v[4:5], v[194:195], v[68:69] op_sel:[0,1,0]
	s_nop 0
	v_pk_fma_f32 v[64:65], v[46:47], v[196:197], v[64:65] op_sel_hi:[1,0,1]
	v_mov_b32_e32 v196, v197
	v_pk_fma_f32 v[68:69], v[2:3], v[196:197], v[64:65] op_sel_hi:[1,0,1]
	ds_read_b128 v[194:197], v89 offset:10240
	s_waitcnt lgkmcnt(1)
	v_pk_fma_f32 v[68:69], v[48:49], v[198:199], v[68:69] op_sel_hi:[1,0,1]
	s_nop 0
	v_pk_fma_f32 v[64:65], v[12:13], v[198:199], v[68:69] op_sel:[0,1,0]
	s_nop 0
	v_pk_fma_f32 v[64:65], v[50:51], v[200:201], v[64:65] op_sel_hi:[1,0,1]
	v_mov_b32_e32 v200, v201
	v_pk_fma_f32 v[68:69], v[10:11], v[200:201], v[64:65] op_sel_hi:[1,0,1]
	ds_read_b128 v[198:201], v89 offset:11264
	s_waitcnt lgkmcnt(1)
	v_pk_fma_f32 v[68:69], v[52:53], v[194:195], v[68:69] op_sel_hi:[1,0,1]
	s_nop 0
	v_pk_fma_f32 v[64:65], v[42:43], v[194:195], v[68:69] op_sel:[0,1,0]
	s_nop 0
	v_pk_fma_f32 v[64:65], v[54:55], v[196:197], v[64:65] op_sel_hi:[1,0,1]
	v_mov_b32_e32 v196, v197
	v_pk_fma_f32 v[68:69], v[40:41], v[196:197], v[64:65] op_sel_hi:[1,0,1]
	ds_read_b128 v[194:197], v89 offset:12288
	s_waitcnt lgkmcnt(1)
	v_pk_fma_f32 v[68:69], v[56:57], v[198:199], v[68:69] op_sel_hi:[1,0,1]
	s_nop 0
	v_pk_fma_f32 v[64:65], v[8:9], v[198:199], v[68:69] op_sel:[0,1,0]
	s_nop 0
	v_pk_fma_f32 v[64:65], v[58:59], v[200:201], v[64:65] op_sel_hi:[1,0,1]
	v_mov_b32_e32 v200, v201
	v_pk_fma_f32 v[64:65], v[6:7], v[200:201], v[64:65] op_sel_hi:[1,0,1]
	ds_read_b128 v[198:201], v89 offset:13312
	s_waitcnt lgkmcnt(1)
	v_pk_fma_f32 v[70:71], v[44:45], v[194:195], 0 op_sel_hi:[1,0,0]
	s_nop 0
	v_pk_fma_f32 v[66:67], v[4:5], v[194:195], v[70:71] op_sel:[0,1,0]
	s_nop 0
	v_pk_fma_f32 v[66:67], v[46:47], v[196:197], v[66:67] op_sel_hi:[1,0,1]
	v_mov_b32_e32 v196, v197
	v_pk_fma_f32 v[70:71], v[2:3], v[196:197], v[66:67] op_sel_hi:[1,0,1]
	ds_read_b128 v[194:197], v89 offset:14336
	s_waitcnt lgkmcnt(1)
	v_pk_fma_f32 v[70:71], v[48:49], v[198:199], v[70:71] op_sel_hi:[1,0,1]
	s_nop 0
	v_pk_fma_f32 v[66:67], v[12:13], v[198:199], v[70:71] op_sel:[0,1,0]
	s_nop 0
	v_pk_fma_f32 v[66:67], v[50:51], v[200:201], v[66:67] op_sel_hi:[1,0,1]
	v_mov_b32_e32 v200, v201
	v_pk_fma_f32 v[70:71], v[10:11], v[200:201], v[66:67] op_sel_hi:[1,0,1]
	ds_read_b128 v[198:201], v89 offset:15360
	s_waitcnt lgkmcnt(1)
	v_pk_fma_f32 v[70:71], v[52:53], v[194:195], v[70:71] op_sel_hi:[1,0,1]
	s_nop 0
	v_pk_fma_f32 v[66:67], v[42:43], v[194:195], v[70:71] op_sel:[0,1,0]
	s_nop 0
	v_pk_fma_f32 v[66:67], v[54:55], v[196:197], v[66:67] op_sel_hi:[1,0,1]
	v_mov_b32_e32 v196, v197
	v_pk_fma_f32 v[70:71], v[40:41], v[196:197], v[66:67] op_sel_hi:[1,0,1]
	ds_read_b128 v[194:197], v89 offset:16384
	s_waitcnt lgkmcnt(1)
	v_pk_fma_f32 v[70:71], v[56:57], v[198:199], v[70:71] op_sel_hi:[1,0,1]
	s_nop 0
	v_pk_fma_f32 v[66:67], v[8:9], v[198:199], v[70:71] op_sel:[0,1,0]
	s_nop 0
	v_pk_fma_f32 v[66:67], v[58:59], v[200:201], v[66:67] op_sel_hi:[1,0,1]
	v_mov_b32_e32 v200, v201
	v_pk_fma_f32 v[66:67], v[6:7], v[200:201], v[66:67] op_sel_hi:[1,0,1]
	ds_read_b128 v[198:201], v89 offset:17408
	s_waitcnt lgkmcnt(1)
	v_pk_fma_f32 v[72:73], v[44:45], v[194:195], 0 op_sel_hi:[1,0,0]
	s_nop 0
	v_pk_fma_f32 v[68:69], v[4:5], v[194:195], v[72:73] op_sel:[0,1,0]
	s_nop 0
	v_pk_fma_f32 v[68:69], v[46:47], v[196:197], v[68:69] op_sel_hi:[1,0,1]
	v_mov_b32_e32 v196, v197
	v_pk_fma_f32 v[72:73], v[2:3], v[196:197], v[68:69] op_sel_hi:[1,0,1]
	ds_read_b128 v[194:197], v89 offset:18432
	s_waitcnt lgkmcnt(1)
	v_pk_fma_f32 v[72:73], v[48:49], v[198:199], v[72:73] op_sel_hi:[1,0,1]
	s_nop 0
	v_pk_fma_f32 v[68:69], v[12:13], v[198:199], v[72:73] op_sel:[0,1,0]
	s_nop 0
	v_pk_fma_f32 v[68:69], v[50:51], v[200:201], v[68:69] op_sel_hi:[1,0,1]
	v_mov_b32_e32 v200, v201
	v_pk_fma_f32 v[72:73], v[10:11], v[200:201], v[68:69] op_sel_hi:[1,0,1]
	ds_read_b128 v[198:201], v89 offset:19456
	s_waitcnt lgkmcnt(1)
	v_pk_fma_f32 v[72:73], v[52:53], v[194:195], v[72:73] op_sel_hi:[1,0,1]
	s_nop 0
	v_pk_fma_f32 v[68:69], v[42:43], v[194:195], v[72:73] op_sel:[0,1,0]
	s_nop 0
	v_pk_fma_f32 v[68:69], v[54:55], v[196:197], v[68:69] op_sel_hi:[1,0,1]
	v_mov_b32_e32 v196, v197
	v_pk_fma_f32 v[72:73], v[40:41], v[196:197], v[68:69] op_sel_hi:[1,0,1]
	ds_read_b128 v[194:197], v89 offset:20480
	s_waitcnt lgkmcnt(1)
	v_pk_fma_f32 v[72:73], v[56:57], v[198:199], v[72:73] op_sel_hi:[1,0,1]
	s_nop 0
	v_pk_fma_f32 v[68:69], v[8:9], v[198:199], v[72:73] op_sel:[0,1,0]
	s_nop 0
	v_pk_fma_f32 v[68:69], v[58:59], v[200:201], v[68:69] op_sel_hi:[1,0,1]
	v_mov_b32_e32 v200, v201
	v_pk_fma_f32 v[68:69], v[6:7], v[200:201], v[68:69] op_sel_hi:[1,0,1]
	ds_read_b128 v[198:201], v89 offset:21504
	s_waitcnt lgkmcnt(1)
	v_pk_fma_f32 v[74:75], v[44:45], v[194:195], 0 op_sel_hi:[1,0,0]
	s_nop 0
	v_pk_fma_f32 v[70:71], v[4:5], v[194:195], v[74:75] op_sel:[0,1,0]
	s_nop 0
	v_pk_fma_f32 v[70:71], v[46:47], v[196:197], v[70:71] op_sel_hi:[1,0,1]
	v_mov_b32_e32 v196, v197
	v_pk_fma_f32 v[74:75], v[2:3], v[196:197], v[70:71] op_sel_hi:[1,0,1]
	ds_read_b128 v[194:197], v89 offset:22528
	s_waitcnt lgkmcnt(1)
	v_pk_fma_f32 v[74:75], v[48:49], v[198:199], v[74:75] op_sel_hi:[1,0,1]
	s_nop 0
	v_pk_fma_f32 v[70:71], v[12:13], v[198:199], v[74:75] op_sel:[0,1,0]
	s_nop 0
	v_pk_fma_f32 v[70:71], v[50:51], v[200:201], v[70:71] op_sel_hi:[1,0,1]
	v_mov_b32_e32 v200, v201
	v_pk_fma_f32 v[74:75], v[10:11], v[200:201], v[70:71] op_sel_hi:[1,0,1]
	ds_read_b128 v[198:201], v89 offset:23552
	s_waitcnt lgkmcnt(1)
	v_pk_fma_f32 v[74:75], v[52:53], v[194:195], v[74:75] op_sel_hi:[1,0,1]
	s_nop 0
	v_pk_fma_f32 v[70:71], v[42:43], v[194:195], v[74:75] op_sel:[0,1,0]
	s_nop 0
	v_pk_fma_f32 v[70:71], v[54:55], v[196:197], v[70:71] op_sel_hi:[1,0,1]
	v_mov_b32_e32 v196, v197
	v_pk_fma_f32 v[74:75], v[40:41], v[196:197], v[70:71] op_sel_hi:[1,0,1]
	ds_read_b128 v[194:197], v89 offset:24576
	s_waitcnt lgkmcnt(1)
	v_pk_fma_f32 v[74:75], v[56:57], v[198:199], v[74:75] op_sel_hi:[1,0,1]
	s_nop 0
	v_pk_fma_f32 v[70:71], v[8:9], v[198:199], v[74:75] op_sel:[0,1,0]
	s_nop 0
	v_pk_fma_f32 v[70:71], v[58:59], v[200:201], v[70:71] op_sel_hi:[1,0,1]
	v_mov_b32_e32 v200, v201
	v_pk_fma_f32 v[70:71], v[6:7], v[200:201], v[70:71] op_sel_hi:[1,0,1]
	ds_read_b128 v[198:201], v89 offset:25600
	s_waitcnt lgkmcnt(1)
	v_pk_fma_f32 v[76:77], v[44:45], v[194:195], 0 op_sel_hi:[1,0,0]
	s_nop 0
	v_pk_fma_f32 v[72:73], v[4:5], v[194:195], v[76:77] op_sel:[0,1,0]
	s_nop 0
	v_pk_fma_f32 v[72:73], v[46:47], v[196:197], v[72:73] op_sel_hi:[1,0,1]
	v_mov_b32_e32 v196, v197
	v_pk_fma_f32 v[76:77], v[2:3], v[196:197], v[72:73] op_sel_hi:[1,0,1]
	ds_read_b128 v[194:197], v89 offset:26624
	s_waitcnt lgkmcnt(1)
	v_pk_fma_f32 v[76:77], v[48:49], v[198:199], v[76:77] op_sel_hi:[1,0,1]
	s_nop 0
	v_pk_fma_f32 v[72:73], v[12:13], v[198:199], v[76:77] op_sel:[0,1,0]
	s_nop 0
	v_pk_fma_f32 v[72:73], v[50:51], v[200:201], v[72:73] op_sel_hi:[1,0,1]
	v_mov_b32_e32 v200, v201
	v_pk_fma_f32 v[76:77], v[10:11], v[200:201], v[72:73] op_sel_hi:[1,0,1]
	ds_read_b128 v[198:201], v89 offset:27648
	s_waitcnt lgkmcnt(1)
	v_pk_fma_f32 v[76:77], v[52:53], v[194:195], v[76:77] op_sel_hi:[1,0,1]
	s_nop 0
	v_pk_fma_f32 v[72:73], v[42:43], v[194:195], v[76:77] op_sel:[0,1,0]
	s_nop 0
	v_pk_fma_f32 v[72:73], v[54:55], v[196:197], v[72:73] op_sel_hi:[1,0,1]
	v_mov_b32_e32 v196, v197
	v_pk_fma_f32 v[76:77], v[40:41], v[196:197], v[72:73] op_sel_hi:[1,0,1]
	ds_read_b128 v[194:197], v89 offset:28672
	s_waitcnt lgkmcnt(1)
	v_pk_fma_f32 v[76:77], v[56:57], v[198:199], v[76:77] op_sel_hi:[1,0,1]
	s_nop 0
	v_pk_fma_f32 v[72:73], v[8:9], v[198:199], v[76:77] op_sel:[0,1,0]
	s_nop 0
	v_pk_fma_f32 v[72:73], v[58:59], v[200:201], v[72:73] op_sel_hi:[1,0,1]
	v_mov_b32_e32 v200, v201
	v_pk_fma_f32 v[72:73], v[6:7], v[200:201], v[72:73] op_sel_hi:[1,0,1]
	ds_read_b128 v[198:201], v89 offset:29696
	s_waitcnt lgkmcnt(1)
	v_pk_fma_f32 v[78:79], v[44:45], v[194:195], 0 op_sel_hi:[1,0,0]
	s_nop 0
	v_pk_fma_f32 v[74:75], v[4:5], v[194:195], v[78:79] op_sel:[0,1,0]
	s_nop 0
	v_pk_fma_f32 v[74:75], v[46:47], v[196:197], v[74:75] op_sel_hi:[1,0,1]
	v_mov_b32_e32 v196, v197
	v_pk_fma_f32 v[78:79], v[2:3], v[196:197], v[74:75] op_sel_hi:[1,0,1]
	ds_read_b128 v[194:197], v89 offset:30720
	s_waitcnt lgkmcnt(1)
	v_pk_fma_f32 v[78:79], v[48:49], v[198:199], v[78:79] op_sel_hi:[1,0,1]
	s_nop 0
	v_pk_fma_f32 v[74:75], v[12:13], v[198:199], v[78:79] op_sel:[0,1,0]
	s_nop 0
	v_pk_fma_f32 v[74:75], v[50:51], v[200:201], v[74:75] op_sel_hi:[1,0,1]
	v_mov_b32_e32 v200, v201
	v_pk_fma_f32 v[78:79], v[10:11], v[200:201], v[74:75] op_sel_hi:[1,0,1]
	ds_read_b128 v[198:201], v89 offset:31744
	s_waitcnt lgkmcnt(1)
	v_pk_fma_f32 v[78:79], v[52:53], v[194:195], v[78:79] op_sel_hi:[1,0,1]
	s_nop 0
	v_pk_fma_f32 v[74:75], v[42:43], v[194:195], v[78:79] op_sel:[0,1,0]
	s_nop 0
	v_pk_fma_f32 v[74:75], v[54:55], v[196:197], v[74:75] op_sel_hi:[1,0,1]
	v_mov_b32_e32 v196, v197
	v_pk_fma_f32 v[78:79], v[40:41], v[196:197], v[74:75] op_sel_hi:[1,0,1]
	ds_read_b128 v[194:197], v89 offset:32768
	s_waitcnt lgkmcnt(1)
	v_pk_fma_f32 v[78:79], v[56:57], v[198:199], v[78:79] op_sel_hi:[1,0,1]
	s_nop 0
	v_pk_fma_f32 v[74:75], v[8:9], v[198:199], v[78:79] op_sel:[0,1,0]
	s_nop 0
	v_pk_fma_f32 v[74:75], v[58:59], v[200:201], v[74:75] op_sel_hi:[1,0,1]
	v_mov_b32_e32 v200, v201
	v_pk_fma_f32 v[74:75], v[6:7], v[200:201], v[74:75] op_sel_hi:[1,0,1]
	ds_read_b128 v[198:201], v89 offset:33792
	s_waitcnt lgkmcnt(1)
	v_pk_fma_f32 v[80:81], v[44:45], v[194:195], 0 op_sel_hi:[1,0,0]
	s_nop 0
	v_pk_fma_f32 v[76:77], v[4:5], v[194:195], v[80:81] op_sel:[0,1,0]
	s_nop 0
	v_pk_fma_f32 v[76:77], v[46:47], v[196:197], v[76:77] op_sel_hi:[1,0,1]
	v_mov_b32_e32 v196, v197
	v_pk_fma_f32 v[80:81], v[2:3], v[196:197], v[76:77] op_sel_hi:[1,0,1]
	ds_read_b128 v[194:197], v89 offset:34816
	s_waitcnt lgkmcnt(1)
	v_pk_fma_f32 v[80:81], v[48:49], v[198:199], v[80:81] op_sel_hi:[1,0,1]
	s_nop 0
	v_pk_fma_f32 v[76:77], v[12:13], v[198:199], v[80:81] op_sel:[0,1,0]
	s_nop 0
	v_pk_fma_f32 v[76:77], v[50:51], v[200:201], v[76:77] op_sel_hi:[1,0,1]
	v_mov_b32_e32 v200, v201
	v_pk_fma_f32 v[80:81], v[10:11], v[200:201], v[76:77] op_sel_hi:[1,0,1]
	ds_read_b128 v[198:201], v89 offset:35840
	s_waitcnt lgkmcnt(1)
	v_pk_fma_f32 v[80:81], v[52:53], v[194:195], v[80:81] op_sel_hi:[1,0,1]
	s_nop 0
	v_pk_fma_f32 v[76:77], v[42:43], v[194:195], v[80:81] op_sel:[0,1,0]
	s_nop 0
	v_pk_fma_f32 v[76:77], v[54:55], v[196:197], v[76:77] op_sel_hi:[1,0,1]
	v_mov_b32_e32 v196, v197
	v_pk_fma_f32 v[80:81], v[40:41], v[196:197], v[76:77] op_sel_hi:[1,0,1]
	ds_read_b128 v[194:197], v89 offset:36864
	s_waitcnt lgkmcnt(1)
	v_pk_fma_f32 v[80:81], v[56:57], v[198:199], v[80:81] op_sel_hi:[1,0,1]
	s_nop 0
	v_pk_fma_f32 v[76:77], v[8:9], v[198:199], v[80:81] op_sel:[0,1,0]
	s_nop 0
	v_pk_fma_f32 v[76:77], v[58:59], v[200:201], v[76:77] op_sel_hi:[1,0,1]
	v_mov_b32_e32 v200, v201
	v_pk_fma_f32 v[76:77], v[6:7], v[200:201], v[76:77] op_sel_hi:[1,0,1]
	ds_read_b128 v[198:201], v89 offset:37888
	s_nop 0
	v_permlane16_swap_b32_e32 v60, v76
	v_add_f32_e32 v60, v60, v76
	v_permlane16_swap_b32_e32 v61, v77
	s_waitcnt lgkmcnt(1)
	v_pk_fma_f32 v[82:83], v[44:45], v[194:195], 0 op_sel_hi:[1,0,0]
	s_nop 0
	v_pk_fma_f32 v[78:79], v[4:5], v[194:195], v[82:83] op_sel:[0,1,0]
	s_nop 0
	v_pk_fma_f32 v[78:79], v[46:47], v[196:197], v[78:79] op_sel_hi:[1,0,1]
	v_mov_b32_e32 v196, v197
	v_pk_fma_f32 v[82:83], v[2:3], v[196:197], v[78:79] op_sel_hi:[1,0,1]
	ds_read_b128 v[194:197], v89 offset:38912
	s_waitcnt lgkmcnt(1)
	v_pk_fma_f32 v[82:83], v[48:49], v[198:199], v[82:83] op_sel_hi:[1,0,1]
	s_nop 0
	v_pk_fma_f32 v[78:79], v[12:13], v[198:199], v[82:83] op_sel:[0,1,0]
	s_nop 0
	v_pk_fma_f32 v[78:79], v[50:51], v[200:201], v[78:79] op_sel_hi:[1,0,1]
	v_mov_b32_e32 v200, v201
	v_pk_fma_f32 v[82:83], v[10:11], v[200:201], v[78:79] op_sel_hi:[1,0,1]
	ds_read_b128 v[198:201], v89 offset:39936
	s_waitcnt lgkmcnt(1)
	v_pk_fma_f32 v[82:83], v[52:53], v[194:195], v[82:83] op_sel_hi:[1,0,1]
	s_nop 0
	v_pk_fma_f32 v[78:79], v[42:43], v[194:195], v[82:83] op_sel:[0,1,0]
	s_nop 0
	v_pk_fma_f32 v[78:79], v[54:55], v[196:197], v[78:79] op_sel_hi:[1,0,1]
	v_mov_b32_e32 v196, v197
	v_pk_fma_f32 v[82:83], v[40:41], v[196:197], v[78:79] op_sel_hi:[1,0,1]
	ds_read_b128 v[194:197], v89 offset:40960
	s_waitcnt lgkmcnt(1)
	v_pk_fma_f32 v[82:83], v[56:57], v[198:199], v[82:83] op_sel_hi:[1,0,1]
	s_nop 0
	v_pk_fma_f32 v[78:79], v[8:9], v[198:199], v[82:83] op_sel:[0,1,0]
	s_nop 0
	v_pk_fma_f32 v[78:79], v[58:59], v[200:201], v[78:79] op_sel_hi:[1,0,1]
	v_mov_b32_e32 v200, v201
	v_pk_fma_f32 v[78:79], v[6:7], v[200:201], v[78:79] op_sel_hi:[1,0,1]
	ds_read_b128 v[198:201], v89 offset:41984
	s_nop 0
	v_permlane16_swap_b32_e32 v62, v78
	v_add_f32_e32 v62, v62, v78
	v_permlane16_swap_b32_e32 v63, v79
	s_waitcnt lgkmcnt(1)
	v_pk_fma_f32 v[84:85], v[44:45], v[194:195], 0 op_sel_hi:[1,0,0]
	s_nop 0
	v_pk_fma_f32 v[80:81], v[4:5], v[194:195], v[84:85] op_sel:[0,1,0]
	s_nop 0
	v_pk_fma_f32 v[80:81], v[46:47], v[196:197], v[80:81] op_sel_hi:[1,0,1]
	v_mov_b32_e32 v196, v197
	v_pk_fma_f32 v[84:85], v[2:3], v[196:197], v[80:81] op_sel_hi:[1,0,1]
	ds_read_b128 v[194:197], v89 offset:43008
	s_waitcnt lgkmcnt(1)
	v_pk_fma_f32 v[84:85], v[48:49], v[198:199], v[84:85] op_sel_hi:[1,0,1]
	s_nop 0
	v_pk_fma_f32 v[80:81], v[12:13], v[198:199], v[84:85] op_sel:[0,1,0]
	s_nop 0
	v_pk_fma_f32 v[80:81], v[50:51], v[200:201], v[80:81] op_sel_hi:[1,0,1]
	v_mov_b32_e32 v200, v201
	v_pk_fma_f32 v[84:85], v[10:11], v[200:201], v[80:81] op_sel_hi:[1,0,1]
	ds_read_b128 v[198:201], v89 offset:44032
	s_waitcnt lgkmcnt(1)
	v_pk_fma_f32 v[84:85], v[52:53], v[194:195], v[84:85] op_sel_hi:[1,0,1]
	s_nop 0
	v_pk_fma_f32 v[80:81], v[42:43], v[194:195], v[84:85] op_sel:[0,1,0]
	s_nop 0
	v_pk_fma_f32 v[80:81], v[54:55], v[196:197], v[80:81] op_sel_hi:[1,0,1]
	v_mov_b32_e32 v196, v197
	v_pk_fma_f32 v[84:85], v[40:41], v[196:197], v[80:81] op_sel_hi:[1,0,1]
	ds_read_b128 v[194:197], v89 offset:45056
	s_waitcnt lgkmcnt(1)
	v_pk_fma_f32 v[84:85], v[56:57], v[198:199], v[84:85] op_sel_hi:[1,0,1]
	s_nop 0
	v_pk_fma_f32 v[80:81], v[8:9], v[198:199], v[84:85] op_sel:[0,1,0]
	s_nop 0
	v_pk_fma_f32 v[80:81], v[58:59], v[200:201], v[80:81] op_sel_hi:[1,0,1]
	v_mov_b32_e32 v200, v201
	v_pk_fma_f32 v[80:81], v[6:7], v[200:201], v[80:81] op_sel_hi:[1,0,1]
	ds_read_b128 v[198:201], v89 offset:46080
	s_nop 0
	v_permlane16_swap_b32_e32 v64, v80
	v_add_f32_e32 v64, v64, v80
	v_permlane16_swap_b32_e32 v65, v81
	s_waitcnt lgkmcnt(1)
	v_pk_fma_f32 v[86:87], v[44:45], v[194:195], 0 op_sel_hi:[1,0,0]
	s_nop 0
	v_pk_fma_f32 v[82:83], v[4:5], v[194:195], v[86:87] op_sel:[0,1,0]
	s_nop 0
	v_pk_fma_f32 v[82:83], v[46:47], v[196:197], v[82:83] op_sel_hi:[1,0,1]
	v_mov_b32_e32 v196, v197
	v_pk_fma_f32 v[86:87], v[2:3], v[196:197], v[82:83] op_sel_hi:[1,0,1]
	ds_read_b128 v[194:197], v89 offset:47104
	s_waitcnt lgkmcnt(1)
	v_pk_fma_f32 v[86:87], v[48:49], v[198:199], v[86:87] op_sel_hi:[1,0,1]
	s_nop 0
	v_pk_fma_f32 v[82:83], v[12:13], v[198:199], v[86:87] op_sel:[0,1,0]
	s_nop 0
	v_pk_fma_f32 v[82:83], v[50:51], v[200:201], v[82:83] op_sel_hi:[1,0,1]
	v_mov_b32_e32 v200, v201
	v_pk_fma_f32 v[86:87], v[10:11], v[200:201], v[82:83] op_sel_hi:[1,0,1]
	ds_read_b128 v[198:201], v89 offset:48128
	s_waitcnt lgkmcnt(1)
	v_pk_fma_f32 v[86:87], v[52:53], v[194:195], v[86:87] op_sel_hi:[1,0,1]
	s_nop 0
	v_pk_fma_f32 v[82:83], v[42:43], v[194:195], v[86:87] op_sel:[0,1,0]
	s_nop 0
	v_pk_fma_f32 v[82:83], v[54:55], v[196:197], v[82:83] op_sel_hi:[1,0,1]
	v_mov_b32_e32 v196, v197
	v_pk_fma_f32 v[86:87], v[40:41], v[196:197], v[82:83] op_sel_hi:[1,0,1]
	ds_read_b128 v[194:197], v89 offset:49152
	s_waitcnt lgkmcnt(1)
	v_pk_fma_f32 v[86:87], v[56:57], v[198:199], v[86:87] op_sel_hi:[1,0,1]
	s_nop 0
	v_pk_fma_f32 v[82:83], v[8:9], v[198:199], v[86:87] op_sel:[0,1,0]
	s_nop 0
	v_pk_fma_f32 v[82:83], v[58:59], v[200:201], v[82:83] op_sel_hi:[1,0,1]
	v_mov_b32_e32 v200, v201
	v_pk_fma_f32 v[82:83], v[6:7], v[200:201], v[82:83] op_sel_hi:[1,0,1]
	ds_read_b128 v[198:201], v89 offset:50176
	s_nop 0
	v_permlane16_swap_b32_e32 v66, v82
	v_add_f32_e32 v66, v66, v82
	v_permlane16_swap_b32_e32 v67, v83
	s_waitcnt lgkmcnt(1)
	v_pk_fma_f32 v[164:165], v[44:45], v[194:195], 0 op_sel_hi:[1,0,0]
	s_nop 0
	v_pk_fma_f32 v[84:85], v[4:5], v[194:195], v[164:165] op_sel:[0,1,0]
	s_nop 0
	v_pk_fma_f32 v[84:85], v[46:47], v[196:197], v[84:85] op_sel_hi:[1,0,1]
	v_mov_b32_e32 v196, v197
	v_pk_fma_f32 v[164:165], v[2:3], v[196:197], v[84:85] op_sel_hi:[1,0,1]
	ds_read_b128 v[194:197], v89 offset:51200
	s_waitcnt lgkmcnt(1)
	v_pk_fma_f32 v[164:165], v[48:49], v[198:199], v[164:165] op_sel_hi:[1,0,1]
	s_nop 0
	v_pk_fma_f32 v[84:85], v[12:13], v[198:199], v[164:165] op_sel:[0,1,0]
	s_nop 0
	v_pk_fma_f32 v[84:85], v[50:51], v[200:201], v[84:85] op_sel_hi:[1,0,1]
	v_mov_b32_e32 v200, v201
	v_pk_fma_f32 v[164:165], v[10:11], v[200:201], v[84:85] op_sel_hi:[1,0,1]
	ds_read_b128 v[198:201], v89 offset:52224
	s_waitcnt lgkmcnt(1)
	v_pk_fma_f32 v[164:165], v[52:53], v[194:195], v[164:165] op_sel_hi:[1,0,1]
	s_nop 0
	v_pk_fma_f32 v[84:85], v[42:43], v[194:195], v[164:165] op_sel:[0,1,0]
	s_nop 0
	v_pk_fma_f32 v[84:85], v[54:55], v[196:197], v[84:85] op_sel_hi:[1,0,1]
	v_mov_b32_e32 v196, v197
	v_pk_fma_f32 v[164:165], v[40:41], v[196:197], v[84:85] op_sel_hi:[1,0,1]
	ds_read_b128 v[194:197], v89 offset:53248
	s_waitcnt lgkmcnt(1)
	v_pk_fma_f32 v[164:165], v[56:57], v[198:199], v[164:165] op_sel_hi:[1,0,1]
	s_nop 0
	v_pk_fma_f32 v[84:85], v[8:9], v[198:199], v[164:165] op_sel:[0,1,0]
	v_pk_fma_f32 v[84:85], v[58:59], v[200:201], v[84:85] op_sel_hi:[1,0,1]
	v_mov_b32_e32 v200, v201
	v_pk_fma_f32 v[84:85], v[6:7], v[200:201], v[84:85] op_sel_hi:[1,0,1]
	ds_read_b128 v[198:201], v89 offset:54272
	s_waitcnt lgkmcnt(1)
	v_pk_fma_f32 v[86:87], v[44:45], v[194:195], 0 op_sel_hi:[1,0,0]
	s_nop 0
	v_pk_fma_f32 v[86:87], v[4:5], v[194:195], v[86:87] op_sel:[0,1,0]
	v_mov_b32_e32 v194, v197
	v_pk_fma_f32 v[86:87], v[46:47], v[196:197], v[86:87] op_sel_hi:[1,0,1]
	v_permlane16_swap_b32_e32 v68, v84
	v_pk_fma_f32 v[86:87], v[2:3], v[194:195], v[86:87] op_sel_hi:[1,0,1]
	ds_read_b128 v[194:197], v89 offset:55296
	v_add_f32_e32 v68, v68, v84
	v_cndmask_b32_e64 v76, v60, v68, s[40:41]
	v_cndmask_b32_e64 v60, v68, v60, s[40:41]
	v_permlane16_swap_b32_e32 v69, v85
	s_waitcnt lgkmcnt(1)
	v_pk_fma_f32 v[86:87], v[48:49], v[198:199], v[86:87] op_sel_hi:[1,0,1]
	v_add_f32_dpp v60, v76, v60 row_mirror row_mask:0xf bank_mask:0xf bound_ctrl:1
	v_pk_fma_f32 v[86:87], v[12:13], v[198:199], v[86:87] op_sel:[0,1,0]
	v_mov_b32_e32 v198, v201
	v_pk_fma_f32 v[86:87], v[50:51], v[200:201], v[86:87] op_sel_hi:[1,0,1]
	s_nop 0
	v_pk_fma_f32 v[86:87], v[10:11], v[198:199], v[86:87] op_sel_hi:[1,0,1]
	ds_read_b128 v[198:201], v89 offset:56320
	s_waitcnt lgkmcnt(1)
	v_pk_fma_f32 v[86:87], v[52:53], v[194:195], v[86:87] op_sel_hi:[1,0,1]
	s_nop 0
	v_pk_fma_f32 v[86:87], v[42:43], v[194:195], v[86:87] op_sel:[0,1,0]
	v_mov_b32_e32 v194, v197
	v_pk_fma_f32 v[86:87], v[54:55], v[196:197], v[86:87] op_sel_hi:[1,0,1]
	s_nop 0
	v_pk_fma_f32 v[86:87], v[40:41], v[194:195], v[86:87] op_sel_hi:[1,0,1]
	ds_read_b128 v[194:197], v89 offset:57344
	s_waitcnt lgkmcnt(1)
	v_pk_fma_f32 v[86:87], v[56:57], v[198:199], v[86:87] op_sel_hi:[1,0,1]
	s_nop 0
	v_pk_fma_f32 v[86:87], v[8:9], v[198:199], v[86:87] op_sel:[0,1,0]
	v_mov_b32_e32 v198, v201
	v_pk_fma_f32 v[86:87], v[58:59], v[200:201], v[86:87] op_sel_hi:[1,0,1]
	s_nop 0
	v_pk_fma_f32 v[86:87], v[6:7], v[198:199], v[86:87] op_sel_hi:[1,0,1]
	ds_read_b128 v[198:201], v89 offset:58368
	s_nop 0
	v_permlane16_swap_b32_e32 v70, v86
	v_add_f32_e32 v70, v70, v86
	v_cndmask_b32_e64 v68, v62, v70, s[40:41]
	s_waitcnt lgkmcnt(1)
	v_pk_fma_f32 v[168:169], v[44:45], v[194:195], 0 op_sel_hi:[1,0,0]
	v_cndmask_b32_e64 v62, v70, v62, s[40:41]
	v_pk_fma_f32 v[164:165], v[4:5], v[194:195], v[168:169] op_sel:[0,1,0]
	v_permlane16_swap_b32_e32 v71, v87
	v_pk_fma_f32 v[164:165], v[46:47], v[196:197], v[164:165] op_sel_hi:[1,0,1]
	v_mov_b32_e32 v196, v197
	v_pk_fma_f32 v[168:169], v[2:3], v[196:197], v[164:165] op_sel_hi:[1,0,1]
	ds_read_b128 v[194:197], v89 offset:59392
	v_add_f32_dpp v62, v68, v62 row_mirror row_mask:0xf bank_mask:0xf bound_ctrl:1
	s_waitcnt lgkmcnt(1)
	v_pk_fma_f32 v[168:169], v[48:49], v[198:199], v[168:169] op_sel_hi:[1,0,1]
	s_nop 0
	v_pk_fma_f32 v[164:165], v[12:13], v[198:199], v[168:169] op_sel:[0,1,0]
	s_nop 0
	v_pk_fma_f32 v[164:165], v[50:51], v[200:201], v[164:165] op_sel_hi:[1,0,1]
	v_mov_b32_e32 v200, v201
	v_pk_fma_f32 v[168:169], v[10:11], v[200:201], v[164:165] op_sel_hi:[1,0,1]
	ds_read_b128 v[198:201], v89 offset:60416
	s_waitcnt lgkmcnt(1)
	v_pk_fma_f32 v[168:169], v[52:53], v[194:195], v[168:169] op_sel_hi:[1,0,1]
	s_nop 0
	v_pk_fma_f32 v[164:165], v[42:43], v[194:195], v[168:169] op_sel:[0,1,0]
	s_nop 0
	v_pk_fma_f32 v[164:165], v[54:55], v[196:197], v[164:165] op_sel_hi:[1,0,1]
	v_mov_b32_e32 v196, v197
	v_pk_fma_f32 v[168:169], v[40:41], v[196:197], v[164:165] op_sel_hi:[1,0,1]
	ds_read_b128 v[194:197], v89 offset:61440
	s_waitcnt lgkmcnt(1)
	v_pk_fma_f32 v[168:169], v[56:57], v[198:199], v[168:169] op_sel_hi:[1,0,1]
	s_nop 0
	v_pk_fma_f32 v[164:165], v[8:9], v[198:199], v[168:169] op_sel:[0,1,0]
	s_nop 0
	v_pk_fma_f32 v[164:165], v[58:59], v[200:201], v[164:165] op_sel_hi:[1,0,1]
	v_mov_b32_e32 v200, v201
	v_pk_fma_f32 v[168:169], v[6:7], v[200:201], v[164:165] op_sel_hi:[1,0,1]
	ds_read_b128 v[198:201], v89 offset:62464
	s_nop 0
	v_permlane16_swap_b32_e32 v72, v168
	v_add_f32_e32 v72, v72, v168
	v_cndmask_b32_e64 v68, v64, v72, s[40:41]
	s_waitcnt lgkmcnt(1)
	v_pk_fma_f32 v[170:171], v[44:45], v[194:195], 0 op_sel_hi:[1,0,0]
	v_cndmask_b32_e64 v64, v72, v64, s[40:41]
	v_pk_fma_f32 v[164:165], v[4:5], v[194:195], v[170:171] op_sel:[0,1,0]
	v_permlane16_swap_b32_e32 v73, v169
	v_pk_fma_f32 v[164:165], v[46:47], v[196:197], v[164:165] op_sel_hi:[1,0,1]
	v_mov_b32_e32 v196, v197
	v_pk_fma_f32 v[170:171], v[2:3], v[196:197], v[164:165] op_sel_hi:[1,0,1]
	ds_read_b128 v[194:197], v89 offset:63488
	v_add_f32_dpp v64, v68, v64 row_mirror row_mask:0xf bank_mask:0xf bound_ctrl:1
	s_waitcnt lgkmcnt(1)
	v_pk_fma_f32 v[170:171], v[48:49], v[198:199], v[170:171] op_sel_hi:[1,0,1]
	s_nop 0
	v_pk_fma_f32 v[164:165], v[12:13], v[198:199], v[170:171] op_sel:[0,1,0]
	s_nop 0
	v_pk_fma_f32 v[164:165], v[50:51], v[200:201], v[164:165] op_sel_hi:[1,0,1]
	v_mov_b32_e32 v200, v201
	v_pk_fma_f32 v[170:171], v[10:11], v[200:201], v[164:165] op_sel_hi:[1,0,1]
	ds_read_b128 v[198:201], v89 offset:64512
	s_waitcnt lgkmcnt(1)
	v_pk_fma_f32 v[170:171], v[52:53], v[194:195], v[170:171] op_sel_hi:[1,0,1]
	s_nop 0
	v_pk_fma_f32 v[164:165], v[42:43], v[194:195], v[170:171] op_sel:[0,1,0]
	s_nop 0
	v_pk_fma_f32 v[164:165], v[54:55], v[196:197], v[164:165] op_sel_hi:[1,0,1]
	v_mov_b32_e32 v196, v197
	v_pk_fma_f32 v[170:171], v[40:41], v[196:197], v[164:165] op_sel_hi:[1,0,1]
	ds_read_b128 v[194:197], v90
	s_waitcnt lgkmcnt(1)
	v_pk_fma_f32 v[170:171], v[56:57], v[198:199], v[170:171] op_sel_hi:[1,0,1]
	s_nop 0
	v_pk_fma_f32 v[164:165], v[8:9], v[198:199], v[170:171] op_sel:[0,1,0]
	s_nop 0
	v_pk_fma_f32 v[164:165], v[58:59], v[200:201], v[164:165] op_sel_hi:[1,0,1]
	v_mov_b32_e32 v200, v201
	v_pk_fma_f32 v[164:165], v[6:7], v[200:201], v[164:165] op_sel_hi:[1,0,1]
	s_nop 1
	v_permlane16_swap_b32_e32 v74, v164
	v_add_f32_e32 v74, v74, v164
	v_cndmask_b32_e64 v68, v66, v74, s[40:41]
	v_cndmask_b32_e64 v66, v74, v66, s[40:41]
	v_permlane16_swap_b32_e32 v75, v165
	s_nop 0
	v_add_f32_dpp v66, v68, v66 row_mirror row_mask:0xf bank_mask:0xf bound_ctrl:1
	v_cndmask_b32_e64 v68, v60, v64, s[42:43]
	v_cndmask_b32_e64 v60, v64, v60, s[42:43]
	v_cndmask_b32_e64 v64, v62, v66, s[42:43]
	v_cndmask_b32_e64 v62, v66, v62, s[42:43]
	v_add_f32_dpp v60, v68, v60 row_half_mirror row_mask:0xf bank_mask:0xf bound_ctrl:1
	v_add_f32_e32 v66, v73, v169
	v_add_f32_dpp v62, v64, v62 row_half_mirror row_mask:0xf bank_mask:0xf bound_ctrl:1
	v_cndmask_b32_e64 v64, v60, v62, s[44:45]
	v_cndmask_b32_e64 v60, v62, v60, s[44:45]
	s_nop 1
	v_add_f32_dpp v60, v64, v60 quad_perm:[2,3,0,1] row_mask:0xf bank_mask:0xf bound_ctrl:1
	v_add_f32_e32 v64, v69, v85
	s_nop 0
	v_add_f32_dpp v60, v60, v60 quad_perm:[1,0,3,2] row_mask:0xf bank_mask:0xf bound_ctrl:1
	v_mov_b32_e32 v62, v60
	s_nop 1
	v_permlane32_swap_b32_e32 v60, v62
	v_add_f32_e32 v60, v60, v62
	v_cndmask_b32_e64 v166, 0, v60, s[46:47]
	v_add_f32_e32 v60, v61, v77
	v_add_f32_e32 v61, v63, v79
	v_add_f32_e32 v62, v65, v81
	v_add_f32_e32 v65, v71, v87
	v_cndmask_b32_e64 v68, v60, v64, s[40:41]
	v_cndmask_b32_e64 v60, v64, v60, s[40:41]
	v_cndmask_b32_e64 v64, v61, v65, s[40:41]
	v_cndmask_b32_e64 v61, v65, v61, s[40:41]
	v_add_f32_e32 v63, v67, v83
	v_add_f32_e32 v67, v75, v165
	v_add_f32_dpp v61, v64, v61 row_mirror row_mask:0xf bank_mask:0xf bound_ctrl:1
	v_cndmask_b32_e64 v64, v62, v66, s[40:41]
	v_cndmask_b32_e64 v62, v66, v62, s[40:41]
	v_add_f32_dpp v60, v68, v60 row_mirror row_mask:0xf bank_mask:0xf bound_ctrl:1
	s_nop 0
	v_add_f32_dpp v62, v64, v62 row_mirror row_mask:0xf bank_mask:0xf bound_ctrl:1
	v_cndmask_b32_e64 v64, v63, v67, s[40:41]
	v_cndmask_b32_e64 v63, v67, v63, s[40:41]
	s_nop 1
	v_add_f32_dpp v63, v64, v63 row_mirror row_mask:0xf bank_mask:0xf bound_ctrl:1
	v_cndmask_b32_e64 v64, v60, v62, s[42:43]
	v_cndmask_b32_e64 v60, v62, v60, s[42:43]
	v_cndmask_b32_e64 v62, v61, v63, s[42:43]
	v_cndmask_b32_e64 v61, v63, v61, s[42:43]
	v_add_f32_dpp v60, v64, v60 row_half_mirror row_mask:0xf bank_mask:0xf bound_ctrl:1
	s_nop 0
	v_add_f32_dpp v61, v62, v61 row_half_mirror row_mask:0xf bank_mask:0xf bound_ctrl:1
	v_cndmask_b32_e64 v62, v60, v61, s[44:45]
	v_cndmask_b32_e64 v60, v61, v60, s[44:45]
	s_nop 1
	v_add_f32_dpp v60, v62, v60 quad_perm:[2,3,0,1] row_mask:0xf bank_mask:0xf bound_ctrl:1
	s_nop 1
	v_add_f32_dpp v164, v60, v60 quad_perm:[1,0,3,2] row_mask:0xf bank_mask:0xf bound_ctrl:1
	ds_read_b128 v[198:201], v91
	v_mov_b32_e32 v165, v164
	s_nop 1
	v_permlane32_swap_b32_e32 v164, v165
	s_waitcnt lgkmcnt(1)
	v_pk_fma_f32 v[64:65], v[44:45], v[194:195], 0 op_sel_hi:[1,0,0]
	s_nop 0
	v_pk_fma_f32 v[60:61], v[4:5], v[194:195], v[64:65] op_sel:[0,1,0]
	s_nop 0
	v_pk_fma_f32 v[60:61], v[46:47], v[196:197], v[60:61] op_sel_hi:[1,0,1]
	v_mov_b32_e32 v196, v197
	v_pk_fma_f32 v[64:65], v[2:3], v[196:197], v[60:61] op_sel_hi:[1,0,1]
	ds_read_b128 v[194:197], v92
	s_waitcnt lgkmcnt(1)
	v_pk_fma_f32 v[64:65], v[48:49], v[198:199], v[64:65] op_sel_hi:[1,0,1]
	s_nop 0
	v_pk_fma_f32 v[60:61], v[12:13], v[198:199], v[64:65] op_sel:[0,1,0]
	s_nop 0
	v_pk_fma_f32 v[60:61], v[50:51], v[200:201], v[60:61] op_sel_hi:[1,0,1]
	v_mov_b32_e32 v200, v201
	v_pk_fma_f32 v[64:65], v[10:11], v[200:201], v[60:61] op_sel_hi:[1,0,1]
	ds_read_b128 v[198:201], v93
	s_waitcnt lgkmcnt(1)
	v_pk_fma_f32 v[64:65], v[52:53], v[194:195], v[64:65] op_sel_hi:[1,0,1]
	s_nop 0
	v_pk_fma_f32 v[60:61], v[42:43], v[194:195], v[64:65] op_sel:[0,1,0]
	s_nop 0
	v_pk_fma_f32 v[60:61], v[54:55], v[196:197], v[60:61] op_sel_hi:[1,0,1]
	v_mov_b32_e32 v196, v197
	v_pk_fma_f32 v[64:65], v[40:41], v[196:197], v[60:61] op_sel_hi:[1,0,1]
	ds_read_b128 v[194:197], v94
	s_waitcnt lgkmcnt(1)
	v_pk_fma_f32 v[64:65], v[56:57], v[198:199], v[64:65] op_sel_hi:[1,0,1]
	s_nop 0
	v_pk_fma_f32 v[60:61], v[8:9], v[198:199], v[64:65] op_sel:[0,1,0]
	s_nop 0
	v_pk_fma_f32 v[60:61], v[58:59], v[200:201], v[60:61] op_sel_hi:[1,0,1]
	v_mov_b32_e32 v200, v201
	v_pk_fma_f32 v[60:61], v[6:7], v[200:201], v[60:61] op_sel_hi:[1,0,1]
	ds_read_b128 v[198:201], v95
	s_waitcnt lgkmcnt(1)
	v_pk_fma_f32 v[66:67], v[44:45], v[194:195], 0 op_sel_hi:[1,0,0]
	s_nop 0
	v_pk_fma_f32 v[62:63], v[4:5], v[194:195], v[66:67] op_sel:[0,1,0]
	s_nop 0
	v_pk_fma_f32 v[62:63], v[46:47], v[196:197], v[62:63] op_sel_hi:[1,0,1]
	v_mov_b32_e32 v196, v197
	v_pk_fma_f32 v[66:67], v[2:3], v[196:197], v[62:63] op_sel_hi:[1,0,1]
	ds_read_b128 v[194:197], v96
	s_waitcnt lgkmcnt(1)
	v_pk_fma_f32 v[66:67], v[48:49], v[198:199], v[66:67] op_sel_hi:[1,0,1]
	s_nop 0
	v_pk_fma_f32 v[62:63], v[12:13], v[198:199], v[66:67] op_sel:[0,1,0]
	s_nop 0
	v_pk_fma_f32 v[62:63], v[50:51], v[200:201], v[62:63] op_sel_hi:[1,0,1]
	v_mov_b32_e32 v200, v201
	v_pk_fma_f32 v[66:67], v[10:11], v[200:201], v[62:63] op_sel_hi:[1,0,1]
	ds_read_b128 v[198:201], v97
	s_waitcnt lgkmcnt(1)
	v_pk_fma_f32 v[66:67], v[52:53], v[194:195], v[66:67] op_sel_hi:[1,0,1]
	s_nop 0
	v_pk_fma_f32 v[62:63], v[42:43], v[194:195], v[66:67] op_sel:[0,1,0]
	s_nop 0
	v_pk_fma_f32 v[62:63], v[54:55], v[196:197], v[62:63] op_sel_hi:[1,0,1]
	v_mov_b32_e32 v196, v197
	v_pk_fma_f32 v[66:67], v[40:41], v[196:197], v[62:63] op_sel_hi:[1,0,1]
	ds_read_b128 v[194:197], v98
	s_waitcnt lgkmcnt(1)
	v_pk_fma_f32 v[66:67], v[56:57], v[198:199], v[66:67] op_sel_hi:[1,0,1]
	s_nop 0
	v_pk_fma_f32 v[62:63], v[8:9], v[198:199], v[66:67] op_sel:[0,1,0]
	s_nop 0
	v_pk_fma_f32 v[62:63], v[58:59], v[200:201], v[62:63] op_sel_hi:[1,0,1]
	v_mov_b32_e32 v200, v201
	v_pk_fma_f32 v[62:63], v[6:7], v[200:201], v[62:63] op_sel_hi:[1,0,1]
	ds_read_b128 v[198:201], v99
	s_waitcnt lgkmcnt(1)
	v_pk_fma_f32 v[68:69], v[44:45], v[194:195], 0 op_sel_hi:[1,0,0]
	s_nop 0
	v_pk_fma_f32 v[64:65], v[4:5], v[194:195], v[68:69] op_sel:[0,1,0]
	s_nop 0
	v_pk_fma_f32 v[64:65], v[46:47], v[196:197], v[64:65] op_sel_hi:[1,0,1]
	v_mov_b32_e32 v196, v197
	v_pk_fma_f32 v[68:69], v[2:3], v[196:197], v[64:65] op_sel_hi:[1,0,1]
	ds_read_b128 v[194:197], v100
	s_waitcnt lgkmcnt(1)
	v_pk_fma_f32 v[68:69], v[48:49], v[198:199], v[68:69] op_sel_hi:[1,0,1]
	s_nop 0
	v_pk_fma_f32 v[64:65], v[12:13], v[198:199], v[68:69] op_sel:[0,1,0]
	s_nop 0
	v_pk_fma_f32 v[64:65], v[50:51], v[200:201], v[64:65] op_sel_hi:[1,0,1]
	v_mov_b32_e32 v200, v201
	v_pk_fma_f32 v[68:69], v[10:11], v[200:201], v[64:65] op_sel_hi:[1,0,1]
	ds_read_b128 v[198:201], v102
	s_waitcnt lgkmcnt(1)
	v_pk_fma_f32 v[68:69], v[52:53], v[194:195], v[68:69] op_sel_hi:[1,0,1]
	s_nop 0
	v_pk_fma_f32 v[64:65], v[42:43], v[194:195], v[68:69] op_sel:[0,1,0]
	s_nop 0
	v_pk_fma_f32 v[64:65], v[54:55], v[196:197], v[64:65] op_sel_hi:[1,0,1]
	v_mov_b32_e32 v196, v197
	v_pk_fma_f32 v[68:69], v[40:41], v[196:197], v[64:65] op_sel_hi:[1,0,1]
	ds_read_b128 v[194:197], v103
	s_waitcnt lgkmcnt(1)
	v_pk_fma_f32 v[68:69], v[56:57], v[198:199], v[68:69] op_sel_hi:[1,0,1]
	s_nop 0
	v_pk_fma_f32 v[64:65], v[8:9], v[198:199], v[68:69] op_sel:[0,1,0]
	s_nop 0
	v_pk_fma_f32 v[64:65], v[58:59], v[200:201], v[64:65] op_sel_hi:[1,0,1]
	v_mov_b32_e32 v200, v201
	v_pk_fma_f32 v[64:65], v[6:7], v[200:201], v[64:65] op_sel_hi:[1,0,1]
	ds_read_b128 v[198:201], v104
	s_waitcnt lgkmcnt(1)
	v_pk_fma_f32 v[70:71], v[44:45], v[194:195], 0 op_sel_hi:[1,0,0]
	s_nop 0
	v_pk_fma_f32 v[66:67], v[4:5], v[194:195], v[70:71] op_sel:[0,1,0]
	s_nop 0
	v_pk_fma_f32 v[66:67], v[46:47], v[196:197], v[66:67] op_sel_hi:[1,0,1]
	v_mov_b32_e32 v196, v197
	v_pk_fma_f32 v[70:71], v[2:3], v[196:197], v[66:67] op_sel_hi:[1,0,1]
	ds_read_b128 v[194:197], v105
	s_waitcnt lgkmcnt(1)
	v_pk_fma_f32 v[70:71], v[48:49], v[198:199], v[70:71] op_sel_hi:[1,0,1]
	s_nop 0
	v_pk_fma_f32 v[66:67], v[12:13], v[198:199], v[70:71] op_sel:[0,1,0]
	s_nop 0
	v_pk_fma_f32 v[66:67], v[50:51], v[200:201], v[66:67] op_sel_hi:[1,0,1]
	v_mov_b32_e32 v200, v201
	v_pk_fma_f32 v[70:71], v[10:11], v[200:201], v[66:67] op_sel_hi:[1,0,1]
	ds_read_b128 v[198:201], v106
	s_waitcnt lgkmcnt(1)
	v_pk_fma_f32 v[70:71], v[52:53], v[194:195], v[70:71] op_sel_hi:[1,0,1]
	s_nop 0
	v_pk_fma_f32 v[66:67], v[42:43], v[194:195], v[70:71] op_sel:[0,1,0]
	s_nop 0
	v_pk_fma_f32 v[66:67], v[54:55], v[196:197], v[66:67] op_sel_hi:[1,0,1]
	v_mov_b32_e32 v196, v197
	v_pk_fma_f32 v[70:71], v[40:41], v[196:197], v[66:67] op_sel_hi:[1,0,1]
	ds_read_b128 v[194:197], v107
	s_waitcnt lgkmcnt(1)
	v_pk_fma_f32 v[70:71], v[56:57], v[198:199], v[70:71] op_sel_hi:[1,0,1]
	s_nop 0
	v_pk_fma_f32 v[66:67], v[8:9], v[198:199], v[70:71] op_sel:[0,1,0]
	s_nop 0
	v_pk_fma_f32 v[66:67], v[58:59], v[200:201], v[66:67] op_sel_hi:[1,0,1]
	v_mov_b32_e32 v200, v201
	v_pk_fma_f32 v[66:67], v[6:7], v[200:201], v[66:67] op_sel_hi:[1,0,1]
	ds_read_b128 v[198:201], v108
	s_waitcnt lgkmcnt(1)
	v_pk_fma_f32 v[72:73], v[44:45], v[194:195], 0 op_sel_hi:[1,0,0]
	s_nop 0
	v_pk_fma_f32 v[68:69], v[4:5], v[194:195], v[72:73] op_sel:[0,1,0]
	s_nop 0
	v_pk_fma_f32 v[68:69], v[46:47], v[196:197], v[68:69] op_sel_hi:[1,0,1]
	v_mov_b32_e32 v196, v197
	v_pk_fma_f32 v[72:73], v[2:3], v[196:197], v[68:69] op_sel_hi:[1,0,1]
	ds_read_b128 v[194:197], v109
	s_waitcnt lgkmcnt(1)
	v_pk_fma_f32 v[72:73], v[48:49], v[198:199], v[72:73] op_sel_hi:[1,0,1]
	s_nop 0
	v_pk_fma_f32 v[68:69], v[12:13], v[198:199], v[72:73] op_sel:[0,1,0]
	s_nop 0
	v_pk_fma_f32 v[68:69], v[50:51], v[200:201], v[68:69] op_sel_hi:[1,0,1]
	v_mov_b32_e32 v200, v201
	v_pk_fma_f32 v[72:73], v[10:11], v[200:201], v[68:69] op_sel_hi:[1,0,1]
	ds_read_b128 v[198:201], v110
	s_waitcnt lgkmcnt(1)
	v_pk_fma_f32 v[72:73], v[52:53], v[194:195], v[72:73] op_sel_hi:[1,0,1]
	s_nop 0
	v_pk_fma_f32 v[68:69], v[42:43], v[194:195], v[72:73] op_sel:[0,1,0]
	s_nop 0
	v_pk_fma_f32 v[68:69], v[54:55], v[196:197], v[68:69] op_sel_hi:[1,0,1]
	v_mov_b32_e32 v196, v197
	v_pk_fma_f32 v[72:73], v[40:41], v[196:197], v[68:69] op_sel_hi:[1,0,1]
	ds_read_b128 v[194:197], v111
	s_waitcnt lgkmcnt(1)
	v_pk_fma_f32 v[72:73], v[56:57], v[198:199], v[72:73] op_sel_hi:[1,0,1]
	s_nop 0
	v_pk_fma_f32 v[68:69], v[8:9], v[198:199], v[72:73] op_sel:[0,1,0]
	s_nop 0
	v_pk_fma_f32 v[68:69], v[58:59], v[200:201], v[68:69] op_sel_hi:[1,0,1]
	v_mov_b32_e32 v200, v201
	v_pk_fma_f32 v[68:69], v[6:7], v[200:201], v[68:69] op_sel_hi:[1,0,1]
	ds_read_b128 v[198:201], v112
	s_waitcnt lgkmcnt(1)
	v_pk_fma_f32 v[74:75], v[44:45], v[194:195], 0 op_sel_hi:[1,0,0]
	s_nop 0
	v_pk_fma_f32 v[70:71], v[4:5], v[194:195], v[74:75] op_sel:[0,1,0]
	s_nop 0
	v_pk_fma_f32 v[70:71], v[46:47], v[196:197], v[70:71] op_sel_hi:[1,0,1]
	v_mov_b32_e32 v196, v197
	v_pk_fma_f32 v[74:75], v[2:3], v[196:197], v[70:71] op_sel_hi:[1,0,1]
	ds_read_b128 v[194:197], v113
	s_waitcnt lgkmcnt(1)
	v_pk_fma_f32 v[74:75], v[48:49], v[198:199], v[74:75] op_sel_hi:[1,0,1]
	s_nop 0
	v_pk_fma_f32 v[70:71], v[12:13], v[198:199], v[74:75] op_sel:[0,1,0]
	s_nop 0
	v_pk_fma_f32 v[70:71], v[50:51], v[200:201], v[70:71] op_sel_hi:[1,0,1]
	v_mov_b32_e32 v200, v201
	v_pk_fma_f32 v[74:75], v[10:11], v[200:201], v[70:71] op_sel_hi:[1,0,1]
	ds_read_b128 v[198:201], v114
	s_waitcnt lgkmcnt(1)
	v_pk_fma_f32 v[74:75], v[52:53], v[194:195], v[74:75] op_sel_hi:[1,0,1]
	s_nop 0
	v_pk_fma_f32 v[70:71], v[42:43], v[194:195], v[74:75] op_sel:[0,1,0]
	s_nop 0
	v_pk_fma_f32 v[70:71], v[54:55], v[196:197], v[70:71] op_sel_hi:[1,0,1]
	v_mov_b32_e32 v196, v197
	v_pk_fma_f32 v[74:75], v[40:41], v[196:197], v[70:71] op_sel_hi:[1,0,1]
	ds_read_b128 v[194:197], v115
	s_waitcnt lgkmcnt(1)
	v_pk_fma_f32 v[74:75], v[56:57], v[198:199], v[74:75] op_sel_hi:[1,0,1]
	s_nop 0
	v_pk_fma_f32 v[70:71], v[8:9], v[198:199], v[74:75] op_sel:[0,1,0]
	s_nop 0
	v_pk_fma_f32 v[70:71], v[58:59], v[200:201], v[70:71] op_sel_hi:[1,0,1]
	v_mov_b32_e32 v200, v201
	v_pk_fma_f32 v[70:71], v[6:7], v[200:201], v[70:71] op_sel_hi:[1,0,1]
	ds_read_b128 v[198:201], v116
	s_waitcnt lgkmcnt(1)
	v_pk_fma_f32 v[76:77], v[44:45], v[194:195], 0 op_sel_hi:[1,0,0]
	s_nop 0
	v_pk_fma_f32 v[72:73], v[4:5], v[194:195], v[76:77] op_sel:[0,1,0]
	s_nop 0
	v_pk_fma_f32 v[72:73], v[46:47], v[196:197], v[72:73] op_sel_hi:[1,0,1]
	v_mov_b32_e32 v196, v197
	v_pk_fma_f32 v[76:77], v[2:3], v[196:197], v[72:73] op_sel_hi:[1,0,1]
	ds_read_b128 v[194:197], v117
	s_waitcnt lgkmcnt(1)
	v_pk_fma_f32 v[76:77], v[48:49], v[198:199], v[76:77] op_sel_hi:[1,0,1]
	s_nop 0
	v_pk_fma_f32 v[72:73], v[12:13], v[198:199], v[76:77] op_sel:[0,1,0]
	s_nop 0
	v_pk_fma_f32 v[72:73], v[50:51], v[200:201], v[72:73] op_sel_hi:[1,0,1]
	v_mov_b32_e32 v200, v201
	v_pk_fma_f32 v[76:77], v[10:11], v[200:201], v[72:73] op_sel_hi:[1,0,1]
	ds_read_b128 v[198:201], v118
	s_waitcnt lgkmcnt(1)
	v_pk_fma_f32 v[76:77], v[52:53], v[194:195], v[76:77] op_sel_hi:[1,0,1]
	s_nop 0
	v_pk_fma_f32 v[72:73], v[42:43], v[194:195], v[76:77] op_sel:[0,1,0]
	s_nop 0
	v_pk_fma_f32 v[72:73], v[54:55], v[196:197], v[72:73] op_sel_hi:[1,0,1]
	v_mov_b32_e32 v196, v197
	v_pk_fma_f32 v[76:77], v[40:41], v[196:197], v[72:73] op_sel_hi:[1,0,1]
	ds_read_b128 v[194:197], v119
	s_waitcnt lgkmcnt(1)
	v_pk_fma_f32 v[76:77], v[56:57], v[198:199], v[76:77] op_sel_hi:[1,0,1]
	s_nop 0
	v_pk_fma_f32 v[72:73], v[8:9], v[198:199], v[76:77] op_sel:[0,1,0]
	s_nop 0
	v_pk_fma_f32 v[72:73], v[58:59], v[200:201], v[72:73] op_sel_hi:[1,0,1]
	v_mov_b32_e32 v200, v201
	v_pk_fma_f32 v[72:73], v[6:7], v[200:201], v[72:73] op_sel_hi:[1,0,1]
	ds_read_b128 v[198:201], v120
	s_waitcnt lgkmcnt(1)
	v_pk_fma_f32 v[78:79], v[44:45], v[194:195], 0 op_sel_hi:[1,0,0]
	s_nop 0
	v_pk_fma_f32 v[74:75], v[4:5], v[194:195], v[78:79] op_sel:[0,1,0]
	s_nop 0
	v_pk_fma_f32 v[74:75], v[46:47], v[196:197], v[74:75] op_sel_hi:[1,0,1]
	v_mov_b32_e32 v196, v197
	v_pk_fma_f32 v[78:79], v[2:3], v[196:197], v[74:75] op_sel_hi:[1,0,1]
	ds_read_b128 v[194:197], v121
	s_waitcnt lgkmcnt(1)
	v_pk_fma_f32 v[78:79], v[48:49], v[198:199], v[78:79] op_sel_hi:[1,0,1]
	s_nop 0
	v_pk_fma_f32 v[74:75], v[12:13], v[198:199], v[78:79] op_sel:[0,1,0]
	s_nop 0
	v_pk_fma_f32 v[74:75], v[50:51], v[200:201], v[74:75] op_sel_hi:[1,0,1]
	v_mov_b32_e32 v200, v201
	v_pk_fma_f32 v[78:79], v[10:11], v[200:201], v[74:75] op_sel_hi:[1,0,1]
	ds_read_b128 v[198:201], v122
	s_waitcnt lgkmcnt(1)
	v_pk_fma_f32 v[78:79], v[52:53], v[194:195], v[78:79] op_sel_hi:[1,0,1]
	s_nop 0
	v_pk_fma_f32 v[74:75], v[42:43], v[194:195], v[78:79] op_sel:[0,1,0]
	s_nop 0
	v_pk_fma_f32 v[74:75], v[54:55], v[196:197], v[74:75] op_sel_hi:[1,0,1]
	v_mov_b32_e32 v196, v197
	v_pk_fma_f32 v[78:79], v[40:41], v[196:197], v[74:75] op_sel_hi:[1,0,1]
	ds_read_b128 v[194:197], v123
	s_waitcnt lgkmcnt(1)
	v_pk_fma_f32 v[78:79], v[56:57], v[198:199], v[78:79] op_sel_hi:[1,0,1]
	s_nop 0
	v_pk_fma_f32 v[74:75], v[8:9], v[198:199], v[78:79] op_sel:[0,1,0]
	s_nop 0
	v_pk_fma_f32 v[74:75], v[58:59], v[200:201], v[74:75] op_sel_hi:[1,0,1]
	v_mov_b32_e32 v200, v201
	v_pk_fma_f32 v[74:75], v[6:7], v[200:201], v[74:75] op_sel_hi:[1,0,1]
	ds_read_b128 v[198:201], v124
	s_waitcnt lgkmcnt(1)
	v_pk_fma_f32 v[80:81], v[44:45], v[194:195], 0 op_sel_hi:[1,0,0]
	s_nop 0
	v_pk_fma_f32 v[76:77], v[4:5], v[194:195], v[80:81] op_sel:[0,1,0]
	s_nop 0
	v_pk_fma_f32 v[76:77], v[46:47], v[196:197], v[76:77] op_sel_hi:[1,0,1]
	v_mov_b32_e32 v196, v197
	v_pk_fma_f32 v[80:81], v[2:3], v[196:197], v[76:77] op_sel_hi:[1,0,1]
	ds_read_b128 v[194:197], v125
	s_waitcnt lgkmcnt(1)
	v_pk_fma_f32 v[80:81], v[48:49], v[198:199], v[80:81] op_sel_hi:[1,0,1]
	s_nop 0
	v_pk_fma_f32 v[76:77], v[12:13], v[198:199], v[80:81] op_sel:[0,1,0]
	s_nop 0
	v_pk_fma_f32 v[76:77], v[50:51], v[200:201], v[76:77] op_sel_hi:[1,0,1]
	v_mov_b32_e32 v200, v201
	v_pk_fma_f32 v[80:81], v[10:11], v[200:201], v[76:77] op_sel_hi:[1,0,1]
	ds_read_b128 v[198:201], v126
	s_waitcnt lgkmcnt(1)
	v_pk_fma_f32 v[80:81], v[52:53], v[194:195], v[80:81] op_sel_hi:[1,0,1]
	s_nop 0
	v_pk_fma_f32 v[76:77], v[42:43], v[194:195], v[80:81] op_sel:[0,1,0]
	s_nop 0
	v_pk_fma_f32 v[76:77], v[54:55], v[196:197], v[76:77] op_sel_hi:[1,0,1]
	v_mov_b32_e32 v196, v197
	v_pk_fma_f32 v[80:81], v[40:41], v[196:197], v[76:77] op_sel_hi:[1,0,1]
	ds_read_b128 v[194:197], v127
	s_waitcnt lgkmcnt(1)
	v_pk_fma_f32 v[80:81], v[56:57], v[198:199], v[80:81] op_sel_hi:[1,0,1]
	s_nop 0
	v_pk_fma_f32 v[76:77], v[8:9], v[198:199], v[80:81] op_sel:[0,1,0]
	s_nop 0
	v_pk_fma_f32 v[76:77], v[58:59], v[200:201], v[76:77] op_sel_hi:[1,0,1]
	v_mov_b32_e32 v200, v201
	v_pk_fma_f32 v[76:77], v[6:7], v[200:201], v[76:77] op_sel_hi:[1,0,1]
	ds_read_b128 v[198:201], v128
	s_nop 0
	v_permlane16_swap_b32_e32 v60, v76
	v_permlane16_swap_b32_e32 v61, v77
	s_waitcnt lgkmcnt(1)
	v_pk_fma_f32 v[82:83], v[44:45], v[194:195], 0 op_sel_hi:[1,0,0]
	s_nop 0
	v_pk_fma_f32 v[78:79], v[4:5], v[194:195], v[82:83] op_sel:[0,1,0]
	s_nop 0
	v_pk_fma_f32 v[78:79], v[46:47], v[196:197], v[78:79] op_sel_hi:[1,0,1]
	v_mov_b32_e32 v196, v197
	v_pk_fma_f32 v[82:83], v[2:3], v[196:197], v[78:79] op_sel_hi:[1,0,1]
	ds_read_b128 v[194:197], v129
	s_waitcnt lgkmcnt(1)
	v_pk_fma_f32 v[82:83], v[48:49], v[198:199], v[82:83] op_sel_hi:[1,0,1]
	s_nop 0
	v_pk_fma_f32 v[78:79], v[12:13], v[198:199], v[82:83] op_sel:[0,1,0]
	s_nop 0
	v_pk_fma_f32 v[78:79], v[50:51], v[200:201], v[78:79] op_sel_hi:[1,0,1]
	v_mov_b32_e32 v200, v201
	v_pk_fma_f32 v[82:83], v[10:11], v[200:201], v[78:79] op_sel_hi:[1,0,1]
	ds_read_b128 v[198:201], v130
	s_waitcnt lgkmcnt(1)
	v_pk_fma_f32 v[82:83], v[52:53], v[194:195], v[82:83] op_sel_hi:[1,0,1]
	s_nop 0
	v_pk_fma_f32 v[78:79], v[42:43], v[194:195], v[82:83] op_sel:[0,1,0]
	s_nop 0
	v_pk_fma_f32 v[78:79], v[54:55], v[196:197], v[78:79] op_sel_hi:[1,0,1]
	v_mov_b32_e32 v196, v197
	v_pk_fma_f32 v[82:83], v[40:41], v[196:197], v[78:79] op_sel_hi:[1,0,1]
	ds_read_b128 v[194:197], v131
	s_waitcnt lgkmcnt(1)
	v_pk_fma_f32 v[82:83], v[56:57], v[198:199], v[82:83] op_sel_hi:[1,0,1]
	s_nop 0
	v_pk_fma_f32 v[78:79], v[8:9], v[198:199], v[82:83] op_sel:[0,1,0]
	s_nop 0
	v_pk_fma_f32 v[78:79], v[58:59], v[200:201], v[78:79] op_sel_hi:[1,0,1]
	v_mov_b32_e32 v200, v201
	v_pk_fma_f32 v[78:79], v[6:7], v[200:201], v[78:79] op_sel_hi:[1,0,1]
	ds_read_b128 v[198:201], v132
	s_nop 0
	v_permlane16_swap_b32_e32 v62, v78
	v_permlane16_swap_b32_e32 v63, v79
	s_waitcnt lgkmcnt(1)
	v_pk_fma_f32 v[84:85], v[44:45], v[194:195], 0 op_sel_hi:[1,0,0]
	s_nop 0
	v_pk_fma_f32 v[80:81], v[4:5], v[194:195], v[84:85] op_sel:[0,1,0]
	s_nop 0
	v_pk_fma_f32 v[80:81], v[46:47], v[196:197], v[80:81] op_sel_hi:[1,0,1]
	v_mov_b32_e32 v196, v197
	v_pk_fma_f32 v[84:85], v[2:3], v[196:197], v[80:81] op_sel_hi:[1,0,1]
	ds_read_b128 v[194:197], v133
	s_waitcnt lgkmcnt(1)
	v_pk_fma_f32 v[84:85], v[48:49], v[198:199], v[84:85] op_sel_hi:[1,0,1]
	s_nop 0
	v_pk_fma_f32 v[80:81], v[12:13], v[198:199], v[84:85] op_sel:[0,1,0]
	s_nop 0
	v_pk_fma_f32 v[80:81], v[50:51], v[200:201], v[80:81] op_sel_hi:[1,0,1]
	v_mov_b32_e32 v200, v201
	v_pk_fma_f32 v[84:85], v[10:11], v[200:201], v[80:81] op_sel_hi:[1,0,1]
	ds_read_b128 v[198:201], v134
	s_waitcnt lgkmcnt(1)
	v_pk_fma_f32 v[84:85], v[52:53], v[194:195], v[84:85] op_sel_hi:[1,0,1]
	s_nop 0
	v_pk_fma_f32 v[80:81], v[42:43], v[194:195], v[84:85] op_sel:[0,1,0]
	s_nop 0
	v_pk_fma_f32 v[80:81], v[54:55], v[196:197], v[80:81] op_sel_hi:[1,0,1]
	v_mov_b32_e32 v196, v197
	v_pk_fma_f32 v[84:85], v[40:41], v[196:197], v[80:81] op_sel_hi:[1,0,1]
	ds_read_b128 v[194:197], v135
	s_waitcnt lgkmcnt(1)
	v_pk_fma_f32 v[84:85], v[56:57], v[198:199], v[84:85] op_sel_hi:[1,0,1]
	s_nop 0
	v_pk_fma_f32 v[80:81], v[8:9], v[198:199], v[84:85] op_sel:[0,1,0]
	s_nop 0
	v_pk_fma_f32 v[80:81], v[58:59], v[200:201], v[80:81] op_sel_hi:[1,0,1]
	v_mov_b32_e32 v200, v201
	v_pk_fma_f32 v[80:81], v[6:7], v[200:201], v[80:81] op_sel_hi:[1,0,1]
	ds_read_b128 v[198:201], v136
	s_nop 0
	v_permlane16_swap_b32_e32 v64, v80
	v_permlane16_swap_b32_e32 v65, v81
	s_waitcnt lgkmcnt(1)
	v_pk_fma_f32 v[86:87], v[44:45], v[194:195], 0 op_sel_hi:[1,0,0]
	s_nop 0
	v_pk_fma_f32 v[82:83], v[4:5], v[194:195], v[86:87] op_sel:[0,1,0]
	s_nop 0
	v_pk_fma_f32 v[82:83], v[46:47], v[196:197], v[82:83] op_sel_hi:[1,0,1]
	v_mov_b32_e32 v196, v197
	v_pk_fma_f32 v[86:87], v[2:3], v[196:197], v[82:83] op_sel_hi:[1,0,1]
	ds_read_b128 v[194:197], v137
	s_waitcnt lgkmcnt(1)
	v_pk_fma_f32 v[86:87], v[48:49], v[198:199], v[86:87] op_sel_hi:[1,0,1]
	s_nop 0
	v_pk_fma_f32 v[82:83], v[12:13], v[198:199], v[86:87] op_sel:[0,1,0]
	s_nop 0
	v_pk_fma_f32 v[82:83], v[50:51], v[200:201], v[82:83] op_sel_hi:[1,0,1]
	v_mov_b32_e32 v200, v201
	v_pk_fma_f32 v[86:87], v[10:11], v[200:201], v[82:83] op_sel_hi:[1,0,1]
	ds_read_b128 v[198:201], v138
	s_waitcnt lgkmcnt(1)
	v_pk_fma_f32 v[86:87], v[52:53], v[194:195], v[86:87] op_sel_hi:[1,0,1]
	s_nop 0
	v_pk_fma_f32 v[82:83], v[42:43], v[194:195], v[86:87] op_sel:[0,1,0]
	s_nop 0
	v_pk_fma_f32 v[82:83], v[54:55], v[196:197], v[82:83] op_sel_hi:[1,0,1]
	v_mov_b32_e32 v196, v197
	v_pk_fma_f32 v[86:87], v[40:41], v[196:197], v[82:83] op_sel_hi:[1,0,1]
	ds_read_b128 v[194:197], v139
	s_waitcnt lgkmcnt(1)
	v_pk_fma_f32 v[86:87], v[56:57], v[198:199], v[86:87] op_sel_hi:[1,0,1]
	s_nop 0
	v_pk_fma_f32 v[82:83], v[8:9], v[198:199], v[86:87] op_sel:[0,1,0]
	s_nop 0
	v_pk_fma_f32 v[82:83], v[58:59], v[200:201], v[82:83] op_sel_hi:[1,0,1]
	v_mov_b32_e32 v200, v201
	v_pk_fma_f32 v[82:83], v[6:7], v[200:201], v[82:83] op_sel_hi:[1,0,1]
	ds_read_b128 v[198:201], v140
	s_nop 0
	v_permlane16_swap_b32_e32 v66, v82
	v_permlane16_swap_b32_e32 v67, v83
	s_waitcnt lgkmcnt(1)
	v_pk_fma_f32 v[168:169], v[44:45], v[194:195], 0 op_sel_hi:[1,0,0]
	s_nop 0
	v_pk_fma_f32 v[84:85], v[4:5], v[194:195], v[168:169] op_sel:[0,1,0]
	s_nop 0
	v_pk_fma_f32 v[84:85], v[46:47], v[196:197], v[84:85] op_sel_hi:[1,0,1]
	v_mov_b32_e32 v196, v197
	v_pk_fma_f32 v[168:169], v[2:3], v[196:197], v[84:85] op_sel_hi:[1,0,1]
	ds_read_b128 v[194:197], v141
	s_waitcnt lgkmcnt(1)
	v_pk_fma_f32 v[168:169], v[48:49], v[198:199], v[168:169] op_sel_hi:[1,0,1]
	s_nop 0
	v_pk_fma_f32 v[84:85], v[12:13], v[198:199], v[168:169] op_sel:[0,1,0]
	s_nop 0
	v_pk_fma_f32 v[84:85], v[50:51], v[200:201], v[84:85] op_sel_hi:[1,0,1]
	v_mov_b32_e32 v200, v201
	v_pk_fma_f32 v[168:169], v[10:11], v[200:201], v[84:85] op_sel_hi:[1,0,1]
	ds_read_b128 v[198:201], v142
	s_waitcnt lgkmcnt(1)
	v_pk_fma_f32 v[168:169], v[52:53], v[194:195], v[168:169] op_sel_hi:[1,0,1]
	s_nop 0
	v_pk_fma_f32 v[84:85], v[42:43], v[194:195], v[168:169] op_sel:[0,1,0]
	s_nop 0
	v_pk_fma_f32 v[84:85], v[54:55], v[196:197], v[84:85] op_sel_hi:[1,0,1]
	v_mov_b32_e32 v196, v197
	v_pk_fma_f32 v[168:169], v[40:41], v[196:197], v[84:85] op_sel_hi:[1,0,1]
	ds_read_b128 v[194:197], v143
	s_waitcnt lgkmcnt(1)
	v_pk_fma_f32 v[168:169], v[56:57], v[198:199], v[168:169] op_sel_hi:[1,0,1]
	s_nop 0
	v_pk_fma_f32 v[84:85], v[8:9], v[198:199], v[168:169] op_sel:[0,1,0]
	v_pk_fma_f32 v[84:85], v[58:59], v[200:201], v[84:85] op_sel_hi:[1,0,1]
	v_mov_b32_e32 v200, v201
	v_pk_fma_f32 v[84:85], v[6:7], v[200:201], v[84:85] op_sel_hi:[1,0,1]
	ds_read_b128 v[198:201], v144
	s_waitcnt lgkmcnt(1)
	v_pk_fma_f32 v[86:87], v[44:45], v[194:195], 0 op_sel_hi:[1,0,0]
	s_nop 0
	v_pk_fma_f32 v[86:87], v[4:5], v[194:195], v[86:87] op_sel:[0,1,0]
	v_mov_b32_e32 v194, v197
	v_pk_fma_f32 v[86:87], v[46:47], v[196:197], v[86:87] op_sel_hi:[1,0,1]
	v_permlane16_swap_b32_e32 v68, v84
	v_pk_fma_f32 v[86:87], v[2:3], v[194:195], v[86:87] op_sel_hi:[1,0,1]
	ds_read_b128 v[194:197], v145
	v_permlane16_swap_b32_e32 v69, v85
	s_waitcnt lgkmcnt(1)
	v_pk_fma_f32 v[86:87], v[48:49], v[198:199], v[86:87] op_sel_hi:[1,0,1]
	s_nop 0
	v_pk_fma_f32 v[86:87], v[12:13], v[198:199], v[86:87] op_sel:[0,1,0]
	v_mov_b32_e32 v198, v201
	v_pk_fma_f32 v[86:87], v[50:51], v[200:201], v[86:87] op_sel_hi:[1,0,1]
	s_nop 0
	v_pk_fma_f32 v[86:87], v[10:11], v[198:199], v[86:87] op_sel_hi:[1,0,1]
	ds_read_b128 v[198:201], v146
	s_waitcnt lgkmcnt(1)
	v_pk_fma_f32 v[86:87], v[52:53], v[194:195], v[86:87] op_sel_hi:[1,0,1]
	s_nop 0
	v_pk_fma_f32 v[86:87], v[42:43], v[194:195], v[86:87] op_sel:[0,1,0]
	v_mov_b32_e32 v194, v197
	v_pk_fma_f32 v[86:87], v[54:55], v[196:197], v[86:87] op_sel_hi:[1,0,1]
	s_nop 0
	v_pk_fma_f32 v[86:87], v[40:41], v[194:195], v[86:87] op_sel_hi:[1,0,1]
	ds_read_b128 v[194:197], v147
	s_waitcnt lgkmcnt(1)
	v_pk_fma_f32 v[86:87], v[56:57], v[198:199], v[86:87] op_sel_hi:[1,0,1]
	s_nop 0
	v_pk_fma_f32 v[86:87], v[8:9], v[198:199], v[86:87] op_sel:[0,1,0]
	v_mov_b32_e32 v198, v201
	v_pk_fma_f32 v[86:87], v[58:59], v[200:201], v[86:87] op_sel_hi:[1,0,1]
	s_nop 0
	v_pk_fma_f32 v[86:87], v[6:7], v[198:199], v[86:87] op_sel_hi:[1,0,1]
	ds_read_b128 v[198:201], v148
	s_nop 0
	v_permlane16_swap_b32_e32 v70, v86
	v_permlane16_swap_b32_e32 v71, v87
	s_waitcnt lgkmcnt(1)
	v_pk_fma_f32 v[172:173], v[44:45], v[194:195], 0 op_sel_hi:[1,0,0]
	s_nop 0
	v_pk_fma_f32 v[168:169], v[4:5], v[194:195], v[172:173] op_sel:[0,1,0]
	s_nop 0
	v_pk_fma_f32 v[168:169], v[46:47], v[196:197], v[168:169] op_sel_hi:[1,0,1]
	v_mov_b32_e32 v196, v197
	v_pk_fma_f32 v[172:173], v[2:3], v[196:197], v[168:169] op_sel_hi:[1,0,1]
	ds_read_b128 v[194:197], v149
	s_waitcnt lgkmcnt(1)
	v_pk_fma_f32 v[172:173], v[48:49], v[198:199], v[172:173] op_sel_hi:[1,0,1]
	s_nop 0
	v_pk_fma_f32 v[168:169], v[12:13], v[198:199], v[172:173] op_sel:[0,1,0]
	s_nop 0
	v_pk_fma_f32 v[168:169], v[50:51], v[200:201], v[168:169] op_sel_hi:[1,0,1]
	v_mov_b32_e32 v200, v201
	v_pk_fma_f32 v[172:173], v[10:11], v[200:201], v[168:169] op_sel_hi:[1,0,1]
	ds_read_b128 v[198:201], v150
	s_waitcnt lgkmcnt(1)
	v_pk_fma_f32 v[172:173], v[52:53], v[194:195], v[172:173] op_sel_hi:[1,0,1]
	s_nop 0
	v_pk_fma_f32 v[168:169], v[42:43], v[194:195], v[172:173] op_sel:[0,1,0]
	s_nop 0
	v_pk_fma_f32 v[168:169], v[54:55], v[196:197], v[168:169] op_sel_hi:[1,0,1]
	v_mov_b32_e32 v196, v197
	v_pk_fma_f32 v[172:173], v[40:41], v[196:197], v[168:169] op_sel_hi:[1,0,1]
	ds_read_b128 v[194:197], v151
	s_waitcnt lgkmcnt(1)
	v_pk_fma_f32 v[172:173], v[56:57], v[198:199], v[172:173] op_sel_hi:[1,0,1]
	s_nop 0
	v_pk_fma_f32 v[168:169], v[8:9], v[198:199], v[172:173] op_sel:[0,1,0]
	s_nop 0
	v_pk_fma_f32 v[168:169], v[58:59], v[200:201], v[168:169] op_sel_hi:[1,0,1]
	v_mov_b32_e32 v200, v201
	v_pk_fma_f32 v[172:173], v[6:7], v[200:201], v[168:169] op_sel_hi:[1,0,1]
	ds_read_b128 v[198:201], v152
	s_nop 0
	v_permlane16_swap_b32_e32 v72, v172
	v_permlane16_swap_b32_e32 v73, v173
	s_waitcnt lgkmcnt(1)
	v_pk_fma_f32 v[44:45], v[44:45], v[194:195], 0 op_sel_hi:[1,0,0]
	s_nop 0
	v_pk_fma_f32 v[4:5], v[4:5], v[194:195], v[44:45] op_sel:[0,1,0]
	v_mov_b32_e32 v44, v197
	v_pk_fma_f32 v[4:5], v[46:47], v[196:197], v[4:5] op_sel_hi:[1,0,1]
	s_nop 0
	v_pk_fma_f32 v[44:45], v[2:3], v[44:45], v[4:5] op_sel_hi:[1,0,1]
	ds_read_b128 v[194:197], v153
	s_waitcnt lgkmcnt(1)
	v_pk_fma_f32 v[44:45], v[48:49], v[198:199], v[44:45] op_sel_hi:[1,0,1]
	s_nop 0
	v_pk_fma_f32 v[2:3], v[12:13], v[198:199], v[44:45] op_sel:[0,1,0]
	s_nop 0
	v_pk_fma_f32 v[2:3], v[50:51], v[200:201], v[2:3] op_sel_hi:[1,0,1]
	v_mov_b32_e32 v200, v201
	v_pk_fma_f32 v[10:11], v[10:11], v[200:201], v[2:3] op_sel_hi:[1,0,1]
	ds_read_b128 v[198:201], v154
	s_waitcnt lgkmcnt(1)
	v_pk_fma_f32 v[10:11], v[52:53], v[194:195], v[10:11] op_sel_hi:[1,0,1]
	s_nop 0
	v_pk_fma_f32 v[2:3], v[42:43], v[194:195], v[10:11] op_sel:[0,1,0]
	s_nop 0
	v_pk_fma_f32 v[2:3], v[54:55], v[196:197], v[2:3] op_sel_hi:[1,0,1]
	v_mov_b32_e32 v196, v197
	v_pk_fma_f32 v[10:11], v[40:41], v[196:197], v[2:3] op_sel_hi:[1,0,1]
	s_waitcnt lgkmcnt(0)
	v_pk_fma_f32 v[10:11], v[56:57], v[198:199], v[10:11] op_sel_hi:[1,0,1]
	s_nop 0
	v_pk_fma_f32 v[2:3], v[8:9], v[198:199], v[10:11] op_sel:[0,1,0]
	v_add_f32_e32 v8, v68, v84
	v_pk_fma_f32 v[2:3], v[58:59], v[200:201], v[2:3] op_sel_hi:[1,0,1]
	v_mov_b32_e32 v200, v201
	v_pk_fma_f32 v[2:3], v[6:7], v[200:201], v[2:3] op_sel_hi:[1,0,1]
	v_add_f32_e32 v4, v60, v76
	v_add_f32_e32 v5, v62, v78
	v_add_f32_e32 v9, v70, v86
	v_add_f32_e32 v6, v64, v80
	v_add_f32_e32 v10, v72, v172
	v_permlane16_swap_b32_e32 v74, v2
	v_cndmask_b32_e64 v11, v4, v8, s[40:41]
	v_cndmask_b32_e64 v4, v8, v4, s[40:41]
	v_cndmask_b32_e64 v8, v5, v9, s[40:41]
	v_cndmask_b32_e64 v5, v9, v5, s[40:41]
	v_add_f32_e32 v7, v66, v82
	v_add_f32_e32 v2, v74, v2
	v_add_f32_dpp v5, v8, v5 row_mirror row_mask:0xf bank_mask:0xf bound_ctrl:1
	v_cndmask_b32_e64 v8, v6, v10, s[40:41]
	v_cndmask_b32_e64 v6, v10, v6, s[40:41]
	v_add_f32_dpp v4, v11, v4 row_mirror row_mask:0xf bank_mask:0xf bound_ctrl:1
	v_add_f32_e32 v9, v71, v87
	v_add_f32_dpp v6, v8, v6 row_mirror row_mask:0xf bank_mask:0xf bound_ctrl:1
	v_cndmask_b32_e64 v8, v7, v2, s[40:41]
	v_cndmask_b32_e64 v2, v2, v7, s[40:41]
	v_cndmask_b32_e64 v7, v4, v6, s[42:43]
	v_cndmask_b32_e64 v4, v6, v4, s[42:43]
	v_add_f32_dpp v2, v8, v2 row_mirror row_mask:0xf bank_mask:0xf bound_ctrl:1
	v_cndmask_b32_e64 v6, v5, v2, s[42:43]
	v_cndmask_b32_e64 v2, v2, v5, s[42:43]
	v_add_f32_dpp v4, v7, v4 row_half_mirror row_mask:0xf bank_mask:0xf bound_ctrl:1
	v_add_f32_e32 v8, v69, v85
	v_add_f32_dpp v2, v6, v2 row_half_mirror row_mask:0xf bank_mask:0xf bound_ctrl:1
	v_cndmask_b32_e64 v5, v4, v2, s[44:45]
	v_cndmask_b32_e64 v2, v2, v4, s[44:45]
	v_add_f32_e32 v6, v65, v81
	v_add_f32_e32 v10, v73, v173
	v_add_f32_dpp v2, v5, v2 quad_perm:[2,3,0,1] row_mask:0xf bank_mask:0xf bound_ctrl:1
	v_add_f32_e32 v5, v63, v79
	v_permlane16_swap_b32_e32 v75, v3
	v_add_f32_dpp v2, v2, v2 quad_perm:[1,0,3,2] row_mask:0xf bank_mask:0xf bound_ctrl:1
	v_mov_b32_e32 v4, v2
	s_nop 1
	v_permlane32_swap_b32_e32 v2, v4
	v_add_f32_e32 v2, v2, v4
	v_add_f32_e32 v4, v61, v77
	v_cndmask_b32_e64 v11, v4, v8, s[40:41]
	v_cndmask_b32_e64 v4, v8, v4, s[40:41]
	v_cndmask_b32_e64 v8, v5, v9, s[40:41]
	v_cndmask_b32_e64 v5, v9, v5, s[40:41]
	v_add_f32_e32 v7, v67, v83
	v_add_f32_e32 v3, v75, v3
	v_add_f32_dpp v5, v8, v5 row_mirror row_mask:0xf bank_mask:0xf bound_ctrl:1
	v_cndmask_b32_e64 v8, v6, v10, s[40:41]
	v_cndmask_b32_e64 v6, v10, v6, s[40:41]
	v_add_f32_dpp v4, v11, v4 row_mirror row_mask:0xf bank_mask:0xf bound_ctrl:1
	v_cndmask_b32_e64 v2, v2, v166, s[48:49]
	v_add_f32_dpp v6, v8, v6 row_mirror row_mask:0xf bank_mask:0xf bound_ctrl:1
	v_cndmask_b32_e64 v8, v7, v3, s[40:41]
	v_cndmask_b32_e64 v3, v3, v7, s[40:41]
	v_cndmask_b32_e64 v7, v4, v6, s[42:43]
	v_cndmask_b32_e64 v4, v6, v4, s[42:43]
	v_add_f32_dpp v3, v8, v3 row_mirror row_mask:0xf bank_mask:0xf bound_ctrl:1
	v_cndmask_b32_e64 v6, v5, v3, s[42:43]
	v_cndmask_b32_e64 v3, v3, v5, s[42:43]
	v_add_f32_dpp v4, v7, v4 row_half_mirror row_mask:0xf bank_mask:0xf bound_ctrl:1
	v_add_f32_e32 v2, v88, v2
	v_add_f32_dpp v3, v6, v3 row_half_mirror row_mask:0xf bank_mask:0xf bound_ctrl:1
	v_cndmask_b32_e64 v5, v4, v3, s[44:45]
	v_cndmask_b32_e64 v3, v3, v4, s[44:45]
	s_nop 1
	v_add_f32_dpp v3, v5, v3 quad_perm:[2,3,0,1] row_mask:0xf bank_mask:0xf bound_ctrl:1
	v_mov_b32_dpp v5, v2 quad_perm:[1,0,3,2] row_mask:0xf bank_mask:0xf bound_ctrl:1
	v_max_f32_e32 v5, v5, v5
	v_max_f32_e32 v5, v2, v5
	v_add_f32_dpp v3, v3, v3 quad_perm:[1,0,3,2] row_mask:0xf bank_mask:0xf bound_ctrl:1
	v_mov_b32_e32 v4, v3
	v_mov_b32_dpp v6, v5 quad_perm:[2,3,0,1] row_mask:0xf bank_mask:0xf bound_ctrl:1
	v_max_f32_e32 v6, v6, v6
	v_max_f32_e32 v5, v5, v6
	v_permlane32_swap_b32_e32 v3, v4
	s_nop 0
	v_mov_b32_dpp v6, v5 row_half_mirror row_mask:0xf bank_mask:0xf bound_ctrl:1
	v_max_f32_e32 v6, v6, v6
	v_max_f32_e32 v5, v5, v6
	s_nop 1
	v_mov_b32_dpp v6, v5 row_mirror row_mask:0xf bank_mask:0xf bound_ctrl:1
	v_max_f32_e32 v6, v6, v6
	v_max_f32_e32 v5, v5, v6
	v_mov_b32_e32 v6, v5
	s_nop 1
	v_permlane16_swap_b32_e32 v5, v6
	v_max_f32_e32 v6, v6, v6
	v_max_f32_e32 v5, v5, v5
	v_max_f32_e32 v5, v5, v6
	v_mov_b32_e32 v6, v5
	s_nop 1
	v_permlane32_swap_b32_e32 v5, v6
	v_max_f32_e32 v6, v6, v6
	v_max_f32_e32 v5, v5, v5
	v_max_f32_e32 v5, v5, v6
	v_cmp_eq_f32_e32 vcc, v2, v5
	s_ff1_i32_b64 s0, vcc
	s_lshr_b32 s0, s0, 1
	s_cmp_lg_u64 vcc, 0
	s_cselect_b32 s7, s0, -1
	v_cmp_ne_u32_e32 vcc, s7, v1
	s_nop 1
	v_cndmask_b32_e32 v2, v221, v2, vcc
	s_nop 1
	v_mov_b32_dpp v6, v2 quad_perm:[1,0,3,2] row_mask:0xf bank_mask:0xf bound_ctrl:1
	v_max_f32_e32 v6, v6, v6
	v_max_f32_e32 v6, v2, v6
	s_nop 1
	v_mov_b32_dpp v7, v6 quad_perm:[2,3,0,1] row_mask:0xf bank_mask:0xf bound_ctrl:1
	v_max_f32_e32 v7, v7, v7
	v_max_f32_e32 v6, v6, v7
	s_nop 1
	v_mov_b32_dpp v7, v6 row_half_mirror row_mask:0xf bank_mask:0xf bound_ctrl:1
	v_max_f32_e32 v7, v7, v7
	v_max_f32_e32 v6, v6, v7
	s_nop 1
	v_mov_b32_dpp v7, v6 row_mirror row_mask:0xf bank_mask:0xf bound_ctrl:1
	v_max_f32_e32 v7, v7, v7
	v_max_f32_e32 v6, v6, v7
	v_mov_b32_e32 v7, v6
	s_nop 1
	v_permlane16_swap_b32_e32 v6, v7
	v_max_f32_e32 v7, v7, v7
	v_max_f32_e32 v6, v6, v6
	v_max_f32_e32 v6, v6, v7
	v_mov_b32_e32 v7, v6
	s_nop 1
	v_permlane32_swap_b32_e32 v6, v7
	v_max_f32_e32 v7, v7, v7
	v_max_f32_e32 v6, v6, v6
	v_max_f32_e32 v6, v6, v7
	v_cmp_eq_f32_e32 vcc, v2, v6
	s_ff1_i32_b64 s0, vcc
	s_lshr_b32 s0, s0, 1
	s_cmp_lg_u64 vcc, 0
	s_cselect_b32 s14, s0, -1
	v_cmp_ne_u32_e32 vcc, s14, v1
	s_nop 1
	v_cndmask_b32_e32 v2, v221, v2, vcc
	s_nop 1
	v_mov_b32_dpp v7, v2 quad_perm:[1,0,3,2] row_mask:0xf bank_mask:0xf bound_ctrl:1
	v_max_f32_e32 v7, v7, v7
	v_max_f32_e32 v7, v2, v7
	s_nop 1
	v_mov_b32_dpp v8, v7 quad_perm:[2,3,0,1] row_mask:0xf bank_mask:0xf bound_ctrl:1
	v_max_f32_e32 v8, v8, v8
	v_max_f32_e32 v7, v7, v8
	s_nop 1
	v_mov_b32_dpp v8, v7 row_half_mirror row_mask:0xf bank_mask:0xf bound_ctrl:1
	v_max_f32_e32 v8, v8, v8
	v_max_f32_e32 v7, v7, v8
	s_nop 1
	v_mov_b32_dpp v8, v7 row_mirror row_mask:0xf bank_mask:0xf bound_ctrl:1
	v_max_f32_e32 v8, v8, v8
	v_max_f32_e32 v7, v7, v8
	v_mov_b32_e32 v8, v7
	s_nop 1
	v_permlane16_swap_b32_e32 v7, v8
	v_max_f32_e32 v8, v8, v8
	v_max_f32_e32 v7, v7, v7
	v_max_f32_e32 v7, v7, v8
	v_mov_b32_e32 v8, v7
	s_nop 1
	v_permlane32_swap_b32_e32 v7, v8
	v_max_f32_e32 v8, v8, v8
	v_max_f32_e32 v7, v7, v7
	v_max_f32_e32 v7, v7, v8
	v_cmp_eq_f32_e32 vcc, v2, v7
	s_ff1_i32_b64 s0, vcc
	s_lshr_b32 s0, s0, 1
	s_cmp_lg_u64 vcc, 0
	s_cselect_b32 s15, s0, -1
	v_cmp_ne_u32_e32 vcc, s15, v1
	s_nop 1
	v_cndmask_b32_e32 v2, v221, v2, vcc
	s_nop 1
	v_mov_b32_dpp v8, v2 quad_perm:[1,0,3,2] row_mask:0xf bank_mask:0xf bound_ctrl:1
	v_max_f32_e32 v8, v8, v8
	v_max_f32_e32 v8, v2, v8
	s_nop 1
	v_mov_b32_dpp v9, v8 quad_perm:[2,3,0,1] row_mask:0xf bank_mask:0xf bound_ctrl:1
	v_max_f32_e32 v9, v9, v9
	v_max_f32_e32 v8, v8, v9
	s_nop 1
	v_mov_b32_dpp v9, v8 row_half_mirror row_mask:0xf bank_mask:0xf bound_ctrl:1
	v_max_f32_e32 v9, v9, v9
	v_max_f32_e32 v8, v8, v9
	s_nop 1
	v_mov_b32_dpp v9, v8 row_mirror row_mask:0xf bank_mask:0xf bound_ctrl:1
	v_max_f32_e32 v9, v9, v9
	v_max_f32_e32 v8, v8, v9
	v_mov_b32_e32 v9, v8
	s_nop 1
	v_permlane16_swap_b32_e32 v8, v9
	v_max_f32_e32 v9, v9, v9
	v_max_f32_e32 v8, v8, v8
	v_max_f32_e32 v8, v8, v9
	v_mov_b32_e32 v9, v8
	s_nop 1
	v_permlane32_swap_b32_e32 v8, v9
	v_max_f32_e32 v9, v9, v9
	v_max_f32_e32 v8, v8, v8
	v_max_f32_e32 v8, v8, v9
	v_cmp_eq_f32_e64 s[0:1], v2, v8
	v_add_u32_e32 v2, s27, v159
	s_and_saveexec_b64 s[12:13], s[50:51]
	s_cbranch_execz .LBB0_1366
	v_sub_f32_e32 v6, v6, v5
	v_mul_f32_e32 v6, 0x3fb8aa3b, v6
	v_sub_f32_e32 v7, v7, v5
	v_exp_f32_e32 v6, v6
	v_mul_f32_e32 v7, 0x3fb8aa3b, v7
	v_sub_f32_e32 v5, v8, v5
	v_exp_f32_e32 v7, v7
	v_mul_f32_e32 v5, 0x3fb8aa3b, v5
	v_exp_f32_e32 v5, v5
	v_add_f32_e32 v8, 1.0, v6
	v_add_f32_e32 v8, v8, v7
	v_add_f32_e32 v8, v8, v5
	v_div_scale_f32 v9, s[28:29], v8, v8, 1.0
	v_rcp_f32_e32 v10, v9
	s_ff1_i32_b64 s28, s[0:1]
	s_lshr_b32 s28, s28, 1
	s_cmp_lg_u64 s[0:1], 0
	v_fma_f32 v11, -v9, v10, 1.0
	v_fmac_f32_e32 v10, v11, v10
	v_div_scale_f32 v11, vcc, 1.0, v8, 1.0
	v_mul_f32_e32 v12, v11, v10
	v_fma_f32 v13, -v9, v12, v11
	v_fmac_f32_e32 v12, v13, v10
	v_fma_f32 v9, -v9, v12, v11
	v_div_fmas_f32 v9, v9, v10, v12
	s_cselect_b32 s0, s28, -1
	v_cndmask_b32_e64 v5, v5, v7, s[56:57]
	v_div_fixup_f32 v8, v9, v8, 1.0
	v_mov_b32_e32 v9, s0
	v_mov_b32_e32 v10, s15
	v_cndmask_b32_e64 v5, v5, v6, s[54:55]
	v_cndmask_b32_e64 v9, v9, v10, s[56:57]
	v_mov_b32_e32 v10, s14
	v_cndmask_b32_e64 v5, v5, 1.0, s[52:53]
	v_cndmask_b32_e64 v9, v9, v10, s[54:55]
	v_mov_b32_e32 v10, s7
	v_mul_f32_e32 v5, v8, v5
	v_lshl_add_u64 v[6:7], s[8:9], 4, v[18:19]
	v_cndmask_b32_e64 v9, v9, v10, s[52:53]
	global_store_dword v[6:7], v5, off
	v_add_u32_e32 v5, 0x22300, v2
	ds_write_b32 v5, v9
	v_lshl_add_u32 v5, v9, 2, 0
	v_add_u32_e32 v5, 0x22200, v5
	ds_add_rtn_u32 v5, v5, v210
	v_add_u32_e32 v6, 0x22700, v2
	s_waitcnt lgkmcnt(0)
	ds_write_b32 v6, v5
